# nt hint also on read-once epilogue loads (residual rows, gate/tmp values), gather row loads and the bias-task weight loads
# baseline (speedup 1.0000x reference)
; __global__ void __launch_bounds__(NWAVES * 64, 2) trunk_fwd(Args args) {
;     ...
;         if (wave < 4 && bx >= G - 32 && G >= 32) { const int tk = (bx - (G - 32)) * 4 + wave, l = tk >> 6, kv = (tk >> 5) & 1, n = (tk & 31) * 8 + (lane & 7), k8 = lane >> 3;
;             const float* pe = args.in[kv ? I_PEV : I_PEK] + (size_t)l * 2048; const float* w1 = args.in[kv ? I_VW1 : I_KW1] + (size_t)l * 2048 * 256;
;             float sacc = 0.f;
; #pragma unroll 16
;             for (int k = k8; k < 2048; k += 8) sacc += pe[k] * w1[(size_t)k * 256 + n];
;             sacc += __shfl_xor(sacc, 8); sacc += __shfl_xor(sacc, 16); sacc += __shfl_xor(sacc, 32);
;             if (k8 == 0) CB1[(l * 2 + kv) * 256 + n] = sacc; }
.LBB0_17:
	v_add_co_u32_e32 v10, vcc, 0xfffe2000, v4
	global_load_dword v2, v[6:7], off offset:-480 nt
	global_load_dword v16, v[6:7], off offset:-448 nt
	global_load_dword v17, v[6:7], off offset:-416 nt
	global_load_dword v18, v[6:7], off offset:-384 nt
	global_load_dword v19, v[6:7], off offset:-352 nt
	global_load_dword v20, v[6:7], off offset:-320 nt
	global_load_dword v21, v[6:7], off offset:-288 nt
	global_load_dword v22, v[6:7], off offset:-256 nt
	global_load_dword v23, v[6:7], off offset:-224 nt
	global_load_dword v24, v[6:7], off offset:-192 nt
	global_load_dword v25, v[6:7], off offset:-160 nt
	global_load_dword v26, v[6:7], off offset:-128 nt
	global_load_dword v27, v[6:7], off offset:-96 nt
	global_load_dword v28, v[6:7], off offset:-64 nt
	global_load_dword v29, v[6:7], off offset:-32 nt
	global_load_dword v30, v[6:7], off nt
	v_addc_co_u32_e32 v11, vcc, -1, v5, vcc
	v_add_co_u32_e32 v12, vcc, 0xfffe4000, v4
	v_add_u32_e32 v9, 0x80, v9
	s_nop 0
	v_addc_co_u32_e32 v13, vcc, -1, v5, vcc
	v_add_co_u32_e32 v14, vcc, 0xfffe6000, v4
	global_load_dword v31, v[10:11], off nt
	global_load_dword v32, v[12:13], off nt
	v_addc_co_u32_e32 v15, vcc, -1, v5, vcc
	v_add_co_u32_e32 v10, vcc, 0xfffe8000, v4
	v_lshl_add_u64 v[6:7], v[6:7], 0, s[14:15]
	s_nop 0
	v_addc_co_u32_e32 v11, vcc, -1, v5, vcc
	v_add_co_u32_e32 v12, vcc, 0xfffea000, v4
	global_load_dword v33, v[14:15], off nt
	global_load_dword v34, v[10:11], off nt
	v_addc_co_u32_e32 v13, vcc, -1, v5, vcc
	v_add_co_u32_e32 v10, vcc, 0xfffec000, v4
	s_waitcnt vmcnt(3)
	v_fmac_f32_e32 v3, v2, v31
	v_addc_co_u32_e32 v11, vcc, -1, v5, vcc
	v_add_co_u32_e32 v14, vcc, 0xfffee000, v4
	global_load_dword v35, v[12:13], off nt
	global_load_dword v36, v[10:11], off nt
	v_addc_co_u32_e32 v15, vcc, -1, v5, vcc
	v_add_co_u32_e32 v10, vcc, 0xffff0000, v4
	s_waitcnt vmcnt(4)
	v_fmac_f32_e32 v3, v16, v32
	v_addc_co_u32_e32 v11, vcc, -1, v5, vcc
	v_add_co_u32_e32 v12, vcc, 0xffff2000, v4
	global_load_dword v37, v[14:15], off nt
	global_load_dword v38, v[10:11], off nt
	v_addc_co_u32_e32 v13, vcc, -1, v5, vcc
	v_add_co_u32_e32 v10, vcc, 0xffff4000, v4
	global_load_dword v39, v[12:13], off nt
	s_nop 0
	v_addc_co_u32_e32 v11, vcc, -1, v5, vcc
	v_add_co_u32_e32 v12, vcc, 0xffff6000, v4
	s_waitcnt vmcnt(6)
	v_fmac_f32_e32 v3, v17, v33
	v_addc_co_u32_e32 v13, vcc, -1, v5, vcc
	v_add_co_u32_e32 v14, vcc, 0xffff8000, v4
	global_load_dword v40, v[10:11], off nt
	global_load_dword v41, v[12:13], off nt
	v_addc_co_u32_e32 v15, vcc, -1, v5, vcc
	v_add_co_u32_e32 v10, vcc, 0xffffa000, v4
	s_waitcnt vmcnt(7)
	v_fmac_f32_e32 v3, v18, v34
	v_addc_co_u32_e32 v11, vcc, -1, v5, vcc
	v_add_co_u32_e32 v12, vcc, 0xffffc000, v4
	global_load_dword v42, v[14:15], off nt
	global_load_dword v43, v[10:11], off nt
	v_addc_co_u32_e32 v13, vcc, -1, v5, vcc
	v_add_co_u32_e32 v10, vcc, 0xffffe000, v4
	s_waitcnt vmcnt(8)
	v_fmac_f32_e32 v3, v19, v35
	v_addc_co_u32_e32 v11, vcc, -1, v5, vcc
	global_load_dword v14, v[12:13], off nt
	global_load_dword v15, v[10:11], off nt
	global_load_dword v44, v[4:5], off nt
	s_waitcnt vmcnt(10)
	v_fmac_f32_e32 v3, v20, v36
	v_cmp_lt_u32_e32 vcc, s5, v9
	s_or_b64 s[6:7], vcc, s[6:7]
	v_lshl_add_u64 v[4:5], v[4:5], 0, s[12:13]
	s_waitcnt vmcnt(9)
	v_fmac_f32_e32 v3, v21, v37
	s_waitcnt vmcnt(8)
	v_fmac_f32_e32 v3, v22, v38
	s_waitcnt vmcnt(7)
	v_fmac_f32_e32 v3, v23, v39
	s_waitcnt vmcnt(6)
	v_fmac_f32_e32 v3, v24, v40
	s_waitcnt vmcnt(5)
	v_fmac_f32_e32 v3, v25, v41
	s_waitcnt vmcnt(4)
	v_fmac_f32_e32 v3, v26, v42
	s_waitcnt vmcnt(3)
	v_fmac_f32_e32 v3, v27, v43
	s_waitcnt vmcnt(2)
	v_fmac_f32_e32 v3, v28, v14
	s_waitcnt vmcnt(1)
	v_fmac_f32_e32 v3, v29, v15
	s_waitcnt vmcnt(0)
	v_fmac_f32_e32 v3, v30, v44
	s_andn2_b64 exec, exec, s[6:7]
	s_cbranch_execnz .LBB0_17
	s_or_b64 exec, exec, s[6:7]
	v_mbcnt_lo_u32_b32 v2, -1, 0
	v_mbcnt_hi_u32_b32 v4, -1, v2
	v_and_b32_e32 v5, 64, v4
	v_xor_b32_e32 v2, 8, v4
	v_add_u32_e32 v5, 64, v5
	v_cmp_lt_i32_e32 vcc, v2, v5
	v_xor_b32_e32 v6, 16, v4
	s_nop 0
	v_cndmask_b32_e32 v2, v4, v2, vcc
	v_lshlrev_b32_e32 v2, 2, v2
	ds_bpermute_b32 v2, v2, v3
	v_cmp_lt_i32_e32 vcc, v6, v5
	s_waitcnt lgkmcnt(0)
	v_add_f32_e32 v2, v3, v2
	v_cndmask_b32_e32 v3, v4, v6, vcc
	v_lshlrev_b32_e32 v3, 2, v3
	ds_bpermute_b32 v3, v3, v2
	v_xor_b32_e32 v6, 32, v4
	v_cmp_lt_i32_e32 vcc, v6, v5
	s_waitcnt lgkmcnt(0)
	v_add_f32_e32 v2, v2, v3
	v_cndmask_b32_e32 v3, v4, v6, vcc
	v_lshlrev_b32_e32 v3, 2, v3
	ds_bpermute_b32 v3, v3, v2
	v_cmp_gt_u32_e32 vcc, 8, v1
	s_and_saveexec_b64 s[6:7], vcc
	s_cbranch_execz .LBB0_20
	s_lshl_b32 s2, s4, 9
	s_lshl_b32 s4, s17, 8
	s_or_b32 s2, s4, s2
	s_waitcnt lgkmcnt(0)
	v_add_f32_e32 v4, v2, v3
	v_or_b32_e32 v2, s2, v8
	v_ashrrev_i32_e32 v3, 31, v2
	v_lshl_add_u64 v[2:3], v[2:3], 2, s[30:31]
	v_add_co_u32_e32 v2, vcc, 0x4b20000, v2
	s_nop 1
	v_addc_co_u32_e32 v3, vcc, 0, v3, vcc
	global_store_dword v[2:3], v4, off

; __device__ __forceinline__ unsigned cvt_pk_bf16(float lo, float hi) { f32x2_t v = {lo, hi}; bf16x2_t b = __builtin_convertvector(v, bf16x2_t); return __builtin_bit_cast(unsigned, b); }
;     __device__ __forceinline__ void operator()(const f32x4 (&acc)[2][2][4][2], const Unit& u, int wr, int wc, int fr, int fq) const {
;         const int row0 = u.pm * BM + wr * 64 + fr, col0 = u.pn * BM + wc * 32 + 8 * fq;
;         const int goff = u.be ? ZGB : ZGA;
; #pragma unroll
;         for (int ai = 0; ai < 2; ++ai) {
;             u32x4 gq[4][2], tq[4][2];
; #pragma unroll
;             for (int m = 0; m < 4; ++m) { const size_t row = (size_t)(row0 + ai * HALF + m * 16);
; #pragma unroll
;                 for (int bj = 0; bj < 2; ++bj) { const int c = col0 + bj * HALF;
;                     gq[m][bj] = *(const u32x4*)(Z + row * ZLD + goff + c);
;                     if (u.be != 0) tq[m][bj] = *(const u32x4*)(tmp + row * D + c); } }
; #pragma unroll
;             for (int m = 0; m < 4; ++m) { const size_t row = (size_t)(row0 + ai * HALF + m * 16);
; #pragma unroll
;                 for (int bj = 0; bj < 2; ++bj) { const int c = col0 + bj * HALF; const u32x4 g = gq[m][bj];
;                     f32x4 v0 = acc[ai][bj][m][0] * (f32x4){bflo(g.x), bfhi(g.x), bflo(g.y), bfhi(g.y)};
;                     f32x4 v1 = acc[ai][bj][m][1] * (f32x4){bflo(g.z), bfhi(g.z), bflo(g.w), bfhi(g.w)};
;                     if (u.be != 0) { const u32x4 t = tq[m][bj];
;                         v0 = v0 + (f32x4){bflo(t.x), bfhi(t.x), bflo(t.y), bfhi(t.y)}; v1 = v1 + (f32x4){bflo(t.z), bfhi(t.z), bflo(t.w), bfhi(t.w)}; }
;                     u32x4 w; w.x = cvt_pk_bf16(v0[0], v0[1]); w.y = cvt_pk_bf16(v0[2], v0[3]); w.z = cvt_pk_bf16(v1[0], v1[1]); w.w = cvt_pk_bf16(v1[2], v1[3]);
;                     *(u32x4*)((u.be != 0 ? Y : tmp) + row * D + c) = w; } }
.LBB0_601:
	v_readlane_b32 s14, v252, 62
	v_lshl_or_b32 v130, s49, 8, v206
	v_readlane_b32 s15, v252, 63
	v_lshl_add_u32 v164, s50, 8, v184
	v_ashrrev_i32_e32 v131, 31, v130
	v_mov_b64_e32 v[166:167], s[14:15]
	v_mad_i64_i32 v[132:133], s[14:15], v164, s26, v[166:167]
	v_lshlrev_b64 v[162:163], 1, v[130:131]
	v_lshl_add_u64 v[130:131], v[132:133], 0, v[162:163]
	global_load_dwordx4 v[208:211], v[130:131], off nt
	global_load_dwordx4 v[154:157], v[130:131], off offset:256 nt
	v_or_b32_e32 v130, 16, v164
	v_ashrrev_i32_e32 v131, 31, v130
	v_mad_i64_i32 v[132:133], s[14:15], v130, s26, v[166:167]
	v_lshlrev_b64 v[172:173], 12, v[130:131]
	v_lshl_add_u64 v[130:131], v[132:133], 0, v[162:163]
	global_load_dwordx4 v[150:153], v[130:131], off nt
	global_load_dwordx4 v[146:149], v[130:131], off offset:256 nt
	v_or_b32_e32 v130, 32, v164
	v_ashrrev_i32_e32 v131, 31, v130
	v_mad_i64_i32 v[132:133], s[14:15], v130, s26, v[166:167]
	v_lshlrev_b64 v[170:171], 12, v[130:131]
	v_lshl_add_u64 v[130:131], v[132:133], 0, v[162:163]
	global_load_dwordx4 v[142:145], v[130:131], off nt
	s_nop 0
	global_load_dwordx4 v[130:133], v[130:131], off offset:256 nt
	v_or_b32_e32 v134, 48, v164
	v_ashrrev_i32_e32 v135, 31, v134
	v_mad_i64_i32 v[136:137], s[14:15], v134, s26, v[166:167]
	v_lshlrev_b64 v[168:169], 12, v[134:135]
	v_lshl_add_u64 v[134:135], v[136:137], 0, v[162:163]
	global_load_dwordx4 v[138:141], v[134:135], off nt
	s_nop 0
	global_load_dwordx4 v[134:137], v[134:135], off offset:256 nt
	v_ashrrev_i32_e32 v165, 31, v164
	v_lshlrev_b64 v[212:213], 12, v[164:165]
	s_mov_b64 s[20:21], -1
	s_andn2_b64 vcc, exec, s[4:5]
	s_waitcnt vmcnt(0)
	v_lshlrev_b32_e32 v214, 16, v210
	v_and_b32_e32 v215, 0xffff0000, v210
	v_lshlrev_b32_e32 v210, 16, v211
	v_and_b32_e32 v211, 0xffff0000, v211
	v_pk_mul_f32 v[128:129], v[128:129], v[210:211]
	v_lshlrev_b32_e32 v210, 16, v208
	v_and_b32_e32 v211, 0xffff0000, v208
	v_lshlrev_b32_e32 v208, 16, v209
	v_and_b32_e32 v209, 0xffff0000, v209
	v_pk_mul_f32 v[126:127], v[126:127], v[214:215]
	v_pk_mul_f32 v[124:125], v[124:125], v[208:209]
	v_pk_mul_f32 v[122:123], v[122:123], v[210:211]
	s_nop 0
	v_cvt_pk_bf16_f32 v122, v122, v123
	v_cvt_pk_bf16_f32 v123, v124, v125
	v_cvt_pk_bf16_f32 v124, v126, v127
	v_lshl_add_u64 v[126:127], s[24:25], 0, v[212:213]
	v_cvt_pk_bf16_f32 v125, v128, v129
	v_lshl_add_u64 v[126:127], v[126:127], 0, v[162:163]
	global_store_dwordx4 v[126:127], v[122:125], off
	s_nop 1
	v_lshlrev_b32_e32 v122, 16, v156
	v_and_b32_e32 v123, 0xffff0000, v156
	v_lshlrev_b32_e32 v124, 16, v157
	v_and_b32_e32 v125, 0xffff0000, v157
	v_pk_mul_f32 v[120:121], v[120:121], v[124:125]
	v_pk_mul_f32 v[118:119], v[118:119], v[122:123]
	v_lshlrev_b32_e32 v122, 16, v154
	v_and_b32_e32 v123, 0xffff0000, v154
	v_lshlrev_b32_e32 v124, 16, v155
	v_and_b32_e32 v125, 0xffff0000, v155
	v_pk_mul_f32 v[116:117], v[116:117], v[124:125]
	v_pk_mul_f32 v[114:115], v[114:115], v[122:123]
	s_nop 0
	v_cvt_pk_bf16_f32 v114, v114, v115
	v_cvt_pk_bf16_f32 v115, v116, v117
	v_cvt_pk_bf16_f32 v116, v118, v119
	v_cvt_pk_bf16_f32 v117, v120, v121
	global_store_dwordx4 v[126:127], v[114:117], off offset:256
	s_nop 1
	v_lshlrev_b32_e32 v114, 16, v152
	v_and_b32_e32 v115, 0xffff0000, v152
	v_lshlrev_b32_e32 v116, 16, v153
	v_and_b32_e32 v117, 0xffff0000, v153
	v_pk_mul_f32 v[112:113], v[112:113], v[116:117]
	v_pk_mul_f32 v[110:111], v[110:111], v[114:115]
	v_lshlrev_b32_e32 v114, 16, v150
	v_and_b32_e32 v115, 0xffff0000, v150
	v_lshlrev_b32_e32 v116, 16, v151
	v_and_b32_e32 v117, 0xffff0000, v151
	v_pk_mul_f32 v[108:109], v[108:109], v[116:117]
	v_pk_mul_f32 v[106:107], v[106:107], v[114:115]
	s_nop 0
	v_cvt_pk_bf16_f32 v106, v106, v107
	v_cvt_pk_bf16_f32 v107, v108, v109
	v_cvt_pk_bf16_f32 v108, v110, v111
	v_lshl_add_u64 v[110:111], s[24:25], 0, v[172:173]
	v_cvt_pk_bf16_f32 v109, v112, v113
	v_lshl_add_u64 v[110:111], v[110:111], 0, v[162:163]
	global_store_dwordx4 v[110:111], v[106:109], off
	s_nop 1
	v_lshlrev_b32_e32 v106, 16, v148
	v_and_b32_e32 v107, 0xffff0000, v148
	v_lshlrev_b32_e32 v108, 16, v149
	v_and_b32_e32 v109, 0xffff0000, v149
	v_pk_mul_f32 v[104:105], v[104:105], v[108:109]
	v_pk_mul_f32 v[102:103], v[102:103], v[106:107]
	v_lshlrev_b32_e32 v106, 16, v146
	v_and_b32_e32 v107, 0xffff0000, v146
	v_lshlrev_b32_e32 v108, 16, v147
	v_and_b32_e32 v109, 0xffff0000, v147
	v_pk_mul_f32 v[100:101], v[100:101], v[108:109]
	v_pk_mul_f32 v[98:99], v[98:99], v[106:107]
	s_nop 0
	v_cvt_pk_bf16_f32 v98, v98, v99
	v_cvt_pk_bf16_f32 v99, v100, v101
	v_cvt_pk_bf16_f32 v100, v102, v103
	v_cvt_pk_bf16_f32 v101, v104, v105
	global_store_dwordx4 v[110:111], v[98:101], off offset:256
	s_nop 1
	v_lshlrev_b32_e32 v98, 16, v144
	v_and_b32_e32 v99, 0xffff0000, v144
	v_lshlrev_b32_e32 v100, 16, v145
	v_and_b32_e32 v101, 0xffff0000, v145
	v_pk_mul_f32 v[96:97], v[96:97], v[100:101]
	v_pk_mul_f32 v[94:95], v[94:95], v[98:99]
	v_lshlrev_b32_e32 v98, 16, v142
	v_and_b32_e32 v99, 0xffff0000, v142
	v_lshlrev_b32_e32 v100, 16, v143
	v_and_b32_e32 v101, 0xffff0000, v143
	v_pk_mul_f32 v[92:93], v[92:93], v[100:101]
	v_pk_mul_f32 v[90:91], v[90:91], v[98:99]
	s_nop 0
	v_cvt_pk_bf16_f32 v90, v90, v91
	v_cvt_pk_bf16_f32 v91, v92, v93
	v_cvt_pk_bf16_f32 v92, v94, v95
	v_lshl_add_u64 v[94:95], s[24:25], 0, v[170:171]
	v_cvt_pk_bf16_f32 v93, v96, v97
	v_lshl_add_u64 v[94:95], v[94:95], 0, v[162:163]
	global_store_dwordx4 v[94:95], v[90:93], off
	s_nop 1
	v_lshlrev_b32_e32 v90, 16, v132
	v_and_b32_e32 v91, 0xffff0000, v132
	v_lshlrev_b32_e32 v92, 16, v133
	v_and_b32_e32 v93, 0xffff0000, v133
	v_pk_mul_f32 v[88:89], v[88:89], v[92:93]
	v_pk_mul_f32 v[86:87], v[86:87], v[90:91]
; __device__ __forceinline__ unsigned cvt_pk_bf16(float lo, float hi) { f32x2_t v = {lo, hi}; bf16x2_t b = __builtin_convertvector(v, bf16x2_t); return __builtin_bit_cast(unsigned, b); }
;     __device__ __forceinline__ void operator()(const f32x4 (&acc)[2][2][4][2], const Unit& u, int wr, int wc, int fr, int fq) const {
;     ...
;             for (int m = 0; m < 4; ++m) { const size_t row = (size_t)(row0 + ai * HALF + m * 16);
; #pragma unroll
;                 for (int bj = 0; bj < 2; ++bj) { const int c = col0 + bj * HALF;
;                     gq[m][bj] = *(const u32x4*)(Z + row * ZLD + goff + c);
;                     if (u.be != 0) tq[m][bj] = *(const u32x4*)(tmp + row * D + c); } }
; #pragma unroll
;             for (int m = 0; m < 4; ++m) { const size_t row = (size_t)(row0 + ai * HALF + m * 16);
; #pragma unroll
;                 for (int bj = 0; bj < 2; ++bj) { const int c = col0 + bj * HALF; const u32x4 g = gq[m][bj];
;                     f32x4 v0 = acc[ai][bj][m][0] * (f32x4){bflo(g.x), bfhi(g.x), bflo(g.y), bfhi(g.y)};
;                     f32x4 v1 = acc[ai][bj][m][1] * (f32x4){bflo(g.z), bfhi(g.z), bflo(g.w), bfhi(g.w)};
;                     if (u.be != 0) { const u32x4 t = tq[m][bj];
;                         v0 = v0 + (f32x4){bflo(t.x), bfhi(t.x), bflo(t.y), bfhi(t.y)}; v1 = v1 + (f32x4){bflo(t.z), bfhi(t.z), bflo(t.w), bfhi(t.w)}; }
;                     u32x4 w; w.x = cvt_pk_bf16(v0[0], v0[1]); w.y = cvt_pk_bf16(v0[2], v0[3]); w.z = cvt_pk_bf16(v1[0], v1[1]); w.w = cvt_pk_bf16(v1[2], v1[3]);
;                     *(u32x4*)((u.be != 0 ? Y : tmp) + row * D + c) = w; } }
	v_lshlrev_b32_e32 v90, 16, v130
	v_and_b32_e32 v91, 0xffff0000, v130
	v_lshlrev_b32_e32 v92, 16, v131
	v_and_b32_e32 v93, 0xffff0000, v131
	v_pk_mul_f32 v[84:85], v[84:85], v[92:93]
	v_pk_mul_f32 v[82:83], v[82:83], v[90:91]
	s_nop 0
	v_cvt_pk_bf16_f32 v82, v82, v83
	v_cvt_pk_bf16_f32 v83, v84, v85
	v_cvt_pk_bf16_f32 v84, v86, v87
	v_cvt_pk_bf16_f32 v85, v88, v89
	global_store_dwordx4 v[94:95], v[82:85], off offset:256
	s_nop 1
	v_lshlrev_b32_e32 v82, 16, v140
	v_and_b32_e32 v83, 0xffff0000, v140
	v_lshlrev_b32_e32 v84, 16, v141
	v_and_b32_e32 v85, 0xffff0000, v141
	v_pk_mul_f32 v[80:81], v[80:81], v[84:85]
	v_pk_mul_f32 v[78:79], v[78:79], v[82:83]
	v_lshlrev_b32_e32 v82, 16, v138
	v_and_b32_e32 v83, 0xffff0000, v138
	v_lshlrev_b32_e32 v84, 16, v139
	v_and_b32_e32 v85, 0xffff0000, v139
	v_pk_mul_f32 v[76:77], v[76:77], v[84:85]
	v_pk_mul_f32 v[74:75], v[74:75], v[82:83]
	s_nop 0
	v_cvt_pk_bf16_f32 v74, v74, v75
	v_cvt_pk_bf16_f32 v75, v76, v77
	v_cvt_pk_bf16_f32 v76, v78, v79
	v_lshl_add_u64 v[78:79], s[24:25], 0, v[168:169]
	v_cvt_pk_bf16_f32 v77, v80, v81
	v_lshl_add_u64 v[78:79], v[78:79], 0, v[162:163]
	global_store_dwordx4 v[78:79], v[74:77], off
	s_nop 1
	v_lshlrev_b32_e32 v74, 16, v136
	v_and_b32_e32 v75, 0xffff0000, v136
	v_lshlrev_b32_e32 v76, 16, v137
	v_and_b32_e32 v77, 0xffff0000, v137
	v_pk_mul_f32 v[72:73], v[72:73], v[76:77]
	v_pk_mul_f32 v[70:71], v[70:71], v[74:75]
	v_lshlrev_b32_e32 v74, 16, v134
	v_and_b32_e32 v75, 0xffff0000, v134
	v_lshlrev_b32_e32 v76, 16, v135
	v_and_b32_e32 v77, 0xffff0000, v135
	v_pk_mul_f32 v[68:69], v[68:69], v[76:77]
	v_pk_mul_f32 v[66:67], v[66:67], v[74:75]
	s_nop 0
	v_cvt_pk_bf16_f32 v66, v66, v67
	v_cvt_pk_bf16_f32 v67, v68, v69
	v_cvt_pk_bf16_f32 v68, v70, v71
	v_cvt_pk_bf16_f32 v69, v72, v73
	global_store_dwordx4 v[78:79], v[66:69], off offset:256
	s_nop 1
	v_add_u32_e32 v66, 0x80, v164
	v_ashrrev_i32_e32 v67, 31, v66
	v_mad_i64_i32 v[68:69], s[14:15], v66, s26, v[166:167]
	v_lshlrev_b64 v[98:99], 12, v[66:67]
	v_lshl_add_u64 v[66:67], v[68:69], 0, v[162:163]
	global_load_dwordx4 v[70:73], v[66:67], off nt
	global_load_dwordx4 v[74:77], v[66:67], off offset:256 nt
	v_add_u32_e32 v66, 0x90, v164
	v_ashrrev_i32_e32 v67, 31, v66
	v_mad_i64_i32 v[68:69], s[14:15], v66, s26, v[166:167]
	v_lshlrev_b64 v[100:101], 12, v[66:67]
	v_lshl_add_u64 v[66:67], v[68:69], 0, v[162:163]
	global_load_dwordx4 v[78:81], v[66:67], off nt
	global_load_dwordx4 v[82:85], v[66:67], off offset:256 nt
	v_add_u32_e32 v66, 0xa0, v164
	v_ashrrev_i32_e32 v67, 31, v66
	v_mad_i64_i32 v[68:69], s[14:15], v66, s26, v[166:167]
	v_lshlrev_b64 v[102:103], 12, v[66:67]
	v_lshl_add_u64 v[66:67], v[68:69], 0, v[162:163]
	global_load_dwordx4 v[86:89], v[66:67], off nt
	global_load_dwordx4 v[90:93], v[66:67], off offset:256 nt
	v_add_u32_e32 v66, 0xb0, v164
	v_ashrrev_i32_e32 v67, 31, v66
	v_mad_i64_i32 v[68:69], s[14:15], v66, s26, v[166:167]
	v_lshlrev_b64 v[104:105], 12, v[66:67]
	v_lshl_add_u64 v[66:67], v[68:69], 0, v[162:163]
	global_load_dwordx4 v[94:97], v[66:67], off nt
	s_nop 0
	global_load_dwordx4 v[66:69], v[66:67], off offset:256 nt
	s_waitcnt vmcnt(7)
	v_lshlrev_b32_e32 v106, 16, v72
	v_and_b32_e32 v107, 0xffff0000, v72
	v_lshlrev_b32_e32 v72, 16, v73
	v_and_b32_e32 v73, 0xffff0000, v73
	v_pk_mul_f32 v[64:65], v[64:65], v[72:73]
	v_lshlrev_b32_e32 v72, 16, v70
	v_and_b32_e32 v73, 0xffff0000, v70
	v_lshlrev_b32_e32 v70, 16, v71
	v_and_b32_e32 v71, 0xffff0000, v71
	v_pk_mul_f32 v[62:63], v[62:63], v[106:107]
	v_pk_mul_f32 v[60:61], v[60:61], v[70:71]
	v_pk_mul_f32 v[58:59], v[58:59], v[72:73]
	s_nop 0
	v_cvt_pk_bf16_f32 v58, v58, v59
	v_cvt_pk_bf16_f32 v59, v60, v61
	v_cvt_pk_bf16_f32 v60, v62, v63
	v_lshl_add_u64 v[62:63], s[24:25], 0, v[98:99]
	v_cvt_pk_bf16_f32 v61, v64, v65
	v_lshl_add_u64 v[62:63], v[62:63], 0, v[162:163]
	global_store_dwordx4 v[62:63], v[58:61], off
	s_waitcnt vmcnt(7)
	s_nop 0
	v_lshlrev_b32_e32 v58, 16, v76
	v_and_b32_e32 v59, 0xffff0000, v76
	v_lshlrev_b32_e32 v60, 16, v77
	v_and_b32_e32 v61, 0xffff0000, v77
	v_pk_mul_f32 v[56:57], v[56:57], v[60:61]
	v_pk_mul_f32 v[54:55], v[54:55], v[58:59]
	v_lshlrev_b32_e32 v58, 16, v74
	v_and_b32_e32 v59, 0xffff0000, v74
	v_lshlrev_b32_e32 v60, 16, v75
	v_and_b32_e32 v61, 0xffff0000, v75
	v_pk_mul_f32 v[52:53], v[52:53], v[60:61]
	v_pk_mul_f32 v[50:51], v[50:51], v[58:59]
	s_nop 0
	v_cvt_pk_bf16_f32 v50, v50, v51
	v_cvt_pk_bf16_f32 v51, v52, v53
	v_cvt_pk_bf16_f32 v52, v54, v55
	v_cvt_pk_bf16_f32 v53, v56, v57
	global_store_dwordx4 v[62:63], v[50:53], off offset:256
	s_waitcnt vmcnt(7)
; __device__ __forceinline__ unsigned cvt_pk_bf16(float lo, float hi) { f32x2_t v = {lo, hi}; bf16x2_t b = __builtin_convertvector(v, bf16x2_t); return __builtin_bit_cast(unsigned, b); }
; #define PG8_BAR __builtin_amdgcn_s_barrier()
; template <class Epi, class Sched>
; __device__ __forceinline__ void gemm_phase(LAS unsigned char* lds, const Gemm g, const Sched& S, const Epi& E, const int tid, unsigned* last_sig = nullptr) {
;     ...
;         if (wr == 0) PG8_BAR;
;         E(acc, cur, wr, wc, fr, fq);
;         if (!has_next) break;
; #pragma unroll
;         for (int a = 0; a < 2; ++a)
; #pragma unroll
;             for (int b = 0; b < 2; ++b)
; #pragma unroll
;                 for (int m = 0; m < 4; ++m)
; #pragma unroll
;                     for (int n = 0; n < 2; ++n) acc[a][b][m][n] = (f32x4){0.f, 0.f, 0.f, 0.f};
;         cur = nxt; cA = nA; cB = nB; ++ui;
;         if (wr == 1) PG8_BAR;
;     __device__ __forceinline__ void operator()(const f32x4 (&acc)[2][2][4][2], const Unit& u, int wr, int wc, int fr, int fq) const {
;     ...
;             for (int m = 0; m < 4; ++m) { const size_t row = (size_t)(row0 + ai * HALF + m * 16);
; #pragma unroll
;                 for (int bj = 0; bj < 2; ++bj) { const int c = col0 + bj * HALF; const u32x4 g = gq[m][bj];
;                     f32x4 v0 = acc[ai][bj][m][0] * (f32x4){bflo(g.x), bfhi(g.x), bflo(g.y), bfhi(g.y)};
;                     f32x4 v1 = acc[ai][bj][m][1] * (f32x4){bflo(g.z), bfhi(g.z), bflo(g.w), bfhi(g.w)};
;                     if (u.be != 0) { const u32x4 t = tq[m][bj];
;                         v0 = v0 + (f32x4){bflo(t.x), bfhi(t.x), bflo(t.y), bfhi(t.y)}; v1 = v1 + (f32x4){bflo(t.z), bfhi(t.z), bflo(t.w), bfhi(t.w)}; }
;                     u32x4 w; w.x = cvt_pk_bf16(v0[0], v0[1]); w.y = cvt_pk_bf16(v0[2], v0[3]); w.z = cvt_pk_bf16(v1[0], v1[1]); w.w = cvt_pk_bf16(v1[2], v1[3]);
;                     *(u32x4*)((u.be != 0 ? Y : tmp) + row * D + c) = w; } }
	s_nop 0
	v_lshlrev_b32_e32 v50, 16, v80
	v_and_b32_e32 v51, 0xffff0000, v80
	v_lshlrev_b32_e32 v52, 16, v81
	v_and_b32_e32 v53, 0xffff0000, v81
	v_pk_mul_f32 v[48:49], v[48:49], v[52:53]
	v_pk_mul_f32 v[46:47], v[46:47], v[50:51]
	v_lshlrev_b32_e32 v50, 16, v78
	v_and_b32_e32 v51, 0xffff0000, v78
	v_lshlrev_b32_e32 v52, 16, v79
	v_and_b32_e32 v53, 0xffff0000, v79
	v_pk_mul_f32 v[44:45], v[44:45], v[52:53]
	v_pk_mul_f32 v[42:43], v[42:43], v[50:51]
	s_nop 0
	v_cvt_pk_bf16_f32 v42, v42, v43
	v_cvt_pk_bf16_f32 v43, v44, v45
	v_cvt_pk_bf16_f32 v44, v46, v47
	v_lshl_add_u64 v[46:47], s[24:25], 0, v[100:101]
	v_cvt_pk_bf16_f32 v45, v48, v49
	v_lshl_add_u64 v[46:47], v[46:47], 0, v[162:163]
	global_store_dwordx4 v[46:47], v[42:45], off
	s_waitcnt vmcnt(7)
	s_nop 0
	v_lshlrev_b32_e32 v42, 16, v84
	v_and_b32_e32 v43, 0xffff0000, v84
	v_lshlrev_b32_e32 v44, 16, v85
	v_and_b32_e32 v45, 0xffff0000, v85
	v_pk_mul_f32 v[40:41], v[40:41], v[44:45]
	v_pk_mul_f32 v[38:39], v[38:39], v[42:43]
	v_lshlrev_b32_e32 v42, 16, v82
	v_and_b32_e32 v43, 0xffff0000, v82
	v_lshlrev_b32_e32 v44, 16, v83
	v_and_b32_e32 v45, 0xffff0000, v83
	v_pk_mul_f32 v[36:37], v[36:37], v[44:45]
	v_pk_mul_f32 v[34:35], v[34:35], v[42:43]
	s_nop 0
	v_cvt_pk_bf16_f32 v34, v34, v35
	v_cvt_pk_bf16_f32 v35, v36, v37
	v_cvt_pk_bf16_f32 v36, v38, v39
	v_cvt_pk_bf16_f32 v37, v40, v41
	global_store_dwordx4 v[46:47], v[34:37], off offset:256
	s_waitcnt vmcnt(7)
	s_nop 0
	v_lshlrev_b32_e32 v34, 16, v88
	v_and_b32_e32 v35, 0xffff0000, v88
	v_lshlrev_b32_e32 v36, 16, v89
	v_and_b32_e32 v37, 0xffff0000, v89
	v_pk_mul_f32 v[32:33], v[32:33], v[36:37]
	v_pk_mul_f32 v[30:31], v[30:31], v[34:35]
	v_lshlrev_b32_e32 v34, 16, v86
	v_and_b32_e32 v35, 0xffff0000, v86
	v_lshlrev_b32_e32 v36, 16, v87
	v_and_b32_e32 v37, 0xffff0000, v87
	v_pk_mul_f32 v[28:29], v[28:29], v[36:37]
	v_pk_mul_f32 v[26:27], v[26:27], v[34:35]
	s_nop 0
	v_cvt_pk_bf16_f32 v26, v26, v27
	v_cvt_pk_bf16_f32 v27, v28, v29
	v_cvt_pk_bf16_f32 v28, v30, v31
	v_lshl_add_u64 v[30:31], s[24:25], 0, v[102:103]
	v_cvt_pk_bf16_f32 v29, v32, v33
	v_lshl_add_u64 v[30:31], v[30:31], 0, v[162:163]
	global_store_dwordx4 v[30:31], v[26:29], off
	s_waitcnt vmcnt(7)
	s_nop 0
	v_lshlrev_b32_e32 v26, 16, v92
	v_and_b32_e32 v27, 0xffff0000, v92
	v_lshlrev_b32_e32 v28, 16, v93
	v_and_b32_e32 v29, 0xffff0000, v93
	v_pk_mul_f32 v[24:25], v[24:25], v[28:29]
	v_pk_mul_f32 v[22:23], v[22:23], v[26:27]
	v_lshlrev_b32_e32 v26, 16, v90
	v_and_b32_e32 v27, 0xffff0000, v90
	v_lshlrev_b32_e32 v28, 16, v91
	v_and_b32_e32 v29, 0xffff0000, v91
	v_pk_mul_f32 v[20:21], v[20:21], v[28:29]
	v_pk_mul_f32 v[18:19], v[18:19], v[26:27]
	s_nop 0
	v_cvt_pk_bf16_f32 v18, v18, v19
	v_cvt_pk_bf16_f32 v19, v20, v21
	v_cvt_pk_bf16_f32 v20, v22, v23
	v_cvt_pk_bf16_f32 v21, v24, v25
	global_store_dwordx4 v[30:31], v[18:21], off offset:256
	s_waitcnt vmcnt(7)
	s_nop 0
	v_lshlrev_b32_e32 v18, 16, v96
	v_and_b32_e32 v19, 0xffff0000, v96
	v_lshlrev_b32_e32 v20, 16, v97
	v_and_b32_e32 v21, 0xffff0000, v97
	v_pk_mul_f32 v[16:17], v[16:17], v[20:21]
	v_pk_mul_f32 v[14:15], v[14:15], v[18:19]
	v_lshlrev_b32_e32 v18, 16, v94
	v_and_b32_e32 v19, 0xffff0000, v94
	v_lshlrev_b32_e32 v20, 16, v95
	v_and_b32_e32 v21, 0xffff0000, v95
	v_pk_mul_f32 v[12:13], v[12:13], v[20:21]
	v_pk_mul_f32 v[10:11], v[10:11], v[18:19]
	s_nop 0
	v_cvt_pk_bf16_f32 v10, v10, v11
	v_cvt_pk_bf16_f32 v11, v12, v13
	v_cvt_pk_bf16_f32 v12, v14, v15
	v_lshl_add_u64 v[14:15], s[24:25], 0, v[104:105]
	v_cvt_pk_bf16_f32 v13, v16, v17
	v_lshl_add_u64 v[14:15], v[14:15], 0, v[162:163]
	global_store_dwordx4 v[14:15], v[10:13], off
	s_waitcnt vmcnt(7)
	s_nop 0
	v_lshlrev_b32_e32 v10, 16, v68
	v_and_b32_e32 v11, 0xffff0000, v68
	v_lshlrev_b32_e32 v12, 16, v69
	v_and_b32_e32 v13, 0xffff0000, v69
	v_pk_mul_f32 v[8:9], v[8:9], v[12:13]
	v_pk_mul_f32 v[6:7], v[6:7], v[10:11]
	v_lshlrev_b32_e32 v10, 16, v66
	v_and_b32_e32 v11, 0xffff0000, v66
	v_lshlrev_b32_e32 v12, 16, v67
	v_and_b32_e32 v13, 0xffff0000, v67
	v_pk_mul_f32 v[4:5], v[4:5], v[12:13]
	v_pk_mul_f32 v[2:3], v[2:3], v[10:11]
	s_nop 0
	v_cvt_pk_bf16_f32 v2, v2, v3
	v_cvt_pk_bf16_f32 v3, v4, v5
	v_cvt_pk_bf16_f32 v4, v6, v7
	v_cvt_pk_bf16_f32 v5, v8, v9
	global_store_dwordx4 v[14:15], v[2:5], off offset:256
	s_cbranch_vccnz .LBB0_590
	s_andn2_b64 vcc, exec, s[6:7]
	s_cbranch_vccnz .LBB0_589
	s_barrier
	s_branch .LBB0_589

; __device__ __forceinline__ unsigned cvt_pk_bf16(float lo, float hi) { f32x2_t v = {lo, hi}; bf16x2_t b = __builtin_convertvector(v, bf16x2_t); return __builtin_bit_cast(unsigned, b); }
;     __device__ __forceinline__ void operator()(const f32x4 (&acc)[2][2][4][2], const Unit& u, int wr, int wc, int fr, int fq) const {
;     ...
;             for (int m = 0; m < 4; ++m) { const size_t row = (size_t)(row0 + ai * HALF + m * 16);
; #pragma unroll
;                 for (int bj = 0; bj < 2; ++bj) { const int c = col0 + bj * HALF;
;                     gq[m][bj] = *(const u32x4*)(Z + row * ZLD + goff + c);
;                     if (u.be != 0) tq[m][bj] = *(const u32x4*)(tmp + row * D + c); } }
; #pragma unroll
;             for (int m = 0; m < 4; ++m) { const size_t row = (size_t)(row0 + ai * HALF + m * 16);
; #pragma unroll
;                 for (int bj = 0; bj < 2; ++bj) { const int c = col0 + bj * HALF; const u32x4 g = gq[m][bj];
;                     f32x4 v0 = acc[ai][bj][m][0] * (f32x4){bflo(g.x), bfhi(g.x), bflo(g.y), bfhi(g.y)};
;                     f32x4 v1 = acc[ai][bj][m][1] * (f32x4){bflo(g.z), bfhi(g.z), bflo(g.w), bfhi(g.w)};
;                     if (u.be != 0) { const u32x4 t = tq[m][bj];
;                         v0 = v0 + (f32x4){bflo(t.x), bfhi(t.x), bflo(t.y), bfhi(t.y)}; v1 = v1 + (f32x4){bflo(t.z), bfhi(t.z), bflo(t.w), bfhi(t.w)}; }
;                     u32x4 w; w.x = cvt_pk_bf16(v0[0], v0[1]); w.y = cvt_pk_bf16(v0[2], v0[3]); w.z = cvt_pk_bf16(v1[0], v1[1]); w.w = cvt_pk_bf16(v1[2], v1[3]);
;                     *(u32x4*)((u.be != 0 ? Y : tmp) + row * D + c) = w; } }
.LBB0_621:
	v_readlane_b32 s14, v253, 0
	v_lshl_or_b32 v130, s18, 8, v233
	v_readlane_b32 s15, v253, 1
	v_lshl_add_u32 v212, s20, 8, v1
	v_ashrrev_i32_e32 v131, 31, v130
	v_mov_b64_e32 v[214:215], s[14:15]
	v_ashrrev_i32_e32 v213, 31, v212
	v_mad_i64_i32 v[132:133], s[14:15], v212, s26, v[214:215]
	v_lshlrev_b64 v[210:211], 1, v[130:131]
	v_lshlrev_b64 v[222:223], 12, v[212:213]
	v_lshl_add_u64 v[130:131], v[132:133], 0, v[210:211]
	v_lshl_add_u64 v[134:135], s[24:25], 0, v[222:223]
	global_load_dwordx4 v[236:239], v[130:131], off nt
	v_lshl_add_u64 v[132:133], v[134:135], 0, v[210:211]
	global_load_dwordx4 v[240:243], v[132:133], off nt
	global_load_dwordx4 v[178:181], v[130:131], off offset:256 nt
	global_load_dwordx4 v[182:185], v[132:133], off offset:256 nt
	v_or_b32_e32 v130, 16, v212
	v_ashrrev_i32_e32 v131, 31, v130
	v_mad_i64_i32 v[132:133], s[14:15], v130, s26, v[214:215]
	v_lshlrev_b64 v[220:221], 12, v[130:131]
	v_lshl_add_u64 v[132:133], v[132:133], 0, v[210:211]
	v_lshl_add_u64 v[130:131], s[24:25], 0, v[220:221]
	global_load_dwordx4 v[174:177], v[132:133], off nt
	v_lshl_add_u64 v[130:131], v[130:131], 0, v[210:211]
	global_load_dwordx4 v[170:173], v[130:131], off nt
	global_load_dwordx4 v[154:157], v[132:133], off offset:256 nt
	global_load_dwordx4 v[146:149], v[130:131], off offset:256 nt
	v_or_b32_e32 v130, 32, v212
	v_ashrrev_i32_e32 v131, 31, v130
	v_mad_i64_i32 v[132:133], s[14:15], v130, s26, v[214:215]
	v_lshlrev_b64 v[216:217], 12, v[130:131]
	v_lshl_add_u64 v[132:133], v[132:133], 0, v[210:211]
	v_lshl_add_u64 v[130:131], s[24:25], 0, v[216:217]
	global_load_dwordx4 v[158:161], v[132:133], off nt
	v_lshl_add_u64 v[130:131], v[130:131], 0, v[210:211]
	global_load_dwordx4 v[150:153], v[130:131], off nt
	global_load_dwordx4 v[134:137], v[132:133], off offset:256 nt
	s_nop 0
	global_load_dwordx4 v[130:133], v[130:131], off offset:256 nt
	v_or_b32_e32 v138, 48, v212
	v_ashrrev_i32_e32 v139, 31, v138
	v_mad_i64_i32 v[140:141], s[14:15], v138, s26, v[214:215]
	v_lshlrev_b64 v[218:219], 12, v[138:139]
	v_lshl_add_u64 v[140:141], v[140:141], 0, v[210:211]
	v_lshl_add_u64 v[138:139], s[24:25], 0, v[218:219]
	global_load_dwordx4 v[166:169], v[140:141], off nt
	v_lshl_add_u64 v[138:139], v[138:139], 0, v[210:211]
	global_load_dwordx4 v[162:165], v[138:139], off nt
	global_load_dwordx4 v[142:145], v[140:141], off offset:256 nt
	s_nop 0
	global_load_dwordx4 v[138:141], v[138:139], off offset:256 nt
	v_readlane_b32 s18, v253, 4
	v_readlane_b32 s19, v253, 5
	s_andn2_b64 vcc, exec, s[0:1]
	s_waitcnt vmcnt(0)
	v_lshlrev_b32_e32 v246, 16, v242
	v_lshlrev_b32_e32 v244, 16, v238
	v_and_b32_e32 v245, 0xffff0000, v238
	v_lshlrev_b32_e32 v238, 16, v239
	v_and_b32_e32 v239, 0xffff0000, v239
	v_and_b32_e32 v247, 0xffff0000, v242
	v_lshlrev_b32_e32 v242, 16, v243
	v_and_b32_e32 v243, 0xffff0000, v243
	v_pk_fma_f32 v[128:129], v[128:129], v[238:239], v[242:243]
	v_lshlrev_b32_e32 v238, 16, v236
	v_and_b32_e32 v239, 0xffff0000, v236
	v_lshlrev_b32_e32 v236, 16, v237
	v_and_b32_e32 v237, 0xffff0000, v237
	v_lshlrev_b32_e32 v242, 16, v240
	v_and_b32_e32 v243, 0xffff0000, v240
	v_lshlrev_b32_e32 v240, 16, v241
	v_and_b32_e32 v241, 0xffff0000, v241
	v_pk_fma_f32 v[126:127], v[126:127], v[244:245], v[246:247]
	v_pk_fma_f32 v[124:125], v[124:125], v[236:237], v[240:241]
	v_pk_fma_f32 v[122:123], v[122:123], v[238:239], v[242:243]
	s_nop 0
	v_cvt_pk_bf16_f32 v122, v122, v123
	v_cvt_pk_bf16_f32 v123, v124, v125
	v_cvt_pk_bf16_f32 v124, v126, v127
	v_lshl_add_u64 v[126:127], s[18:19], 0, v[222:223]
	v_cvt_pk_bf16_f32 v125, v128, v129
	v_lshl_add_u64 v[126:127], v[126:127], 0, v[210:211]
	global_store_dwordx4 v[126:127], v[122:125], off
	v_lshlrev_b32_e32 v128, 16, v184
	v_and_b32_e32 v129, 0xffff0000, v184
	v_lshlrev_b32_e32 v122, 16, v180
	v_and_b32_e32 v123, 0xffff0000, v180
	v_lshlrev_b32_e32 v124, 16, v181
	v_and_b32_e32 v125, 0xffff0000, v181
	v_lshlrev_b32_e32 v180, 16, v185
	v_and_b32_e32 v181, 0xffff0000, v185
	v_pk_fma_f32 v[120:121], v[120:121], v[124:125], v[180:181]
	v_pk_fma_f32 v[118:119], v[118:119], v[122:123], v[128:129]
	v_lshlrev_b32_e32 v122, 16, v178
	v_and_b32_e32 v123, 0xffff0000, v178
	v_lshlrev_b32_e32 v124, 16, v179
	v_and_b32_e32 v125, 0xffff0000, v179
	v_lshlrev_b32_e32 v128, 16, v182
	v_and_b32_e32 v129, 0xffff0000, v182
	v_lshlrev_b32_e32 v178, 16, v183
	v_and_b32_e32 v179, 0xffff0000, v183
	v_pk_fma_f32 v[116:117], v[116:117], v[124:125], v[178:179]
	v_pk_fma_f32 v[114:115], v[114:115], v[122:123], v[128:129]
	s_nop 0
	v_cvt_pk_bf16_f32 v114, v114, v115
	v_cvt_pk_bf16_f32 v115, v116, v117
	v_cvt_pk_bf16_f32 v116, v118, v119
	v_cvt_pk_bf16_f32 v117, v120, v121
	global_store_dwordx4 v[126:127], v[114:117], off offset:256
	v_lshlrev_b32_e32 v118, 16, v172
	v_and_b32_e32 v119, 0xffff0000, v172
	v_lshlrev_b32_e32 v114, 16, v176
	v_and_b32_e32 v115, 0xffff0000, v176
	v_lshlrev_b32_e32 v116, 16, v177
	v_and_b32_e32 v117, 0xffff0000, v177
	v_lshlrev_b32_e32 v120, 16, v173
	v_and_b32_e32 v121, 0xffff0000, v173
	v_pk_fma_f32 v[112:113], v[112:113], v[116:117], v[120:121]
	v_pk_fma_f32 v[110:111], v[110:111], v[114:115], v[118:119]
	v_lshlrev_b32_e32 v114, 16, v174
	v_and_b32_e32 v115, 0xffff0000, v174
	v_lshlrev_b32_e32 v116, 16, v175
	v_and_b32_e32 v117, 0xffff0000, v175
	v_lshlrev_b32_e32 v118, 16, v170
	v_and_b32_e32 v119, 0xffff0000, v170
	v_lshlrev_b32_e32 v120, 16, v171
	v_and_b32_e32 v121, 0xffff0000, v171
	v_pk_fma_f32 v[108:109], v[108:109], v[116:117], v[120:121]
	v_pk_fma_f32 v[106:107], v[106:107], v[114:115], v[118:119]
	v_lshlrev_b32_e32 v114, 16, v149
	v_cvt_pk_bf16_f32 v106, v106, v107
	v_cvt_pk_bf16_f32 v107, v108, v109
; __device__ __forceinline__ unsigned cvt_pk_bf16(float lo, float hi) { f32x2_t v = {lo, hi}; bf16x2_t b = __builtin_convertvector(v, bf16x2_t); return __builtin_bit_cast(unsigned, b); }
;     __device__ __forceinline__ void operator()(const f32x4 (&acc)[2][2][4][2], const Unit& u, int wr, int wc, int fr, int fq) const {
;     ...
;             for (int m = 0; m < 4; ++m) { const size_t row = (size_t)(row0 + ai * HALF + m * 16);
; #pragma unroll
;                 for (int bj = 0; bj < 2; ++bj) { const int c = col0 + bj * HALF;
;                     gq[m][bj] = *(const u32x4*)(Z + row * ZLD + goff + c);
;                     if (u.be != 0) tq[m][bj] = *(const u32x4*)(tmp + row * D + c); } }
; #pragma unroll
;             for (int m = 0; m < 4; ++m) { const size_t row = (size_t)(row0 + ai * HALF + m * 16);
; #pragma unroll
;                 for (int bj = 0; bj < 2; ++bj) { const int c = col0 + bj * HALF; const u32x4 g = gq[m][bj];
;                     f32x4 v0 = acc[ai][bj][m][0] * (f32x4){bflo(g.x), bfhi(g.x), bflo(g.y), bfhi(g.y)};
;                     f32x4 v1 = acc[ai][bj][m][1] * (f32x4){bflo(g.z), bfhi(g.z), bflo(g.w), bfhi(g.w)};
;                     if (u.be != 0) { const u32x4 t = tq[m][bj];
;                         v0 = v0 + (f32x4){bflo(t.x), bfhi(t.x), bflo(t.y), bfhi(t.y)}; v1 = v1 + (f32x4){bflo(t.z), bfhi(t.z), bflo(t.w), bfhi(t.w)}; }
;                     u32x4 w; w.x = cvt_pk_bf16(v0[0], v0[1]); w.y = cvt_pk_bf16(v0[2], v0[3]); w.z = cvt_pk_bf16(v1[0], v1[1]); w.w = cvt_pk_bf16(v1[2], v1[3]);
;                     *(u32x4*)((u.be != 0 ? Y : tmp) + row * D + c) = w; } }
	v_cvt_pk_bf16_f32 v108, v110, v111
	v_lshl_add_u64 v[110:111], s[18:19], 0, v[220:221]
	v_cvt_pk_bf16_f32 v109, v112, v113
	v_lshl_add_u64 v[110:111], v[110:111], 0, v[210:211]
	global_store_dwordx4 v[110:111], v[106:109], off
	v_lshlrev_b32_e32 v112, 16, v148
	v_and_b32_e32 v113, 0xffff0000, v148
	v_lshlrev_b32_e32 v106, 16, v156
	v_and_b32_e32 v107, 0xffff0000, v156
	v_lshlrev_b32_e32 v108, 16, v157
	v_and_b32_e32 v109, 0xffff0000, v157
	v_and_b32_e32 v115, 0xffff0000, v149
	v_pk_fma_f32 v[104:105], v[104:105], v[108:109], v[114:115]
	v_pk_fma_f32 v[102:103], v[102:103], v[106:107], v[112:113]
	v_lshlrev_b32_e32 v106, 16, v154
	v_and_b32_e32 v107, 0xffff0000, v154
	v_lshlrev_b32_e32 v108, 16, v155
	v_and_b32_e32 v109, 0xffff0000, v155
	v_lshlrev_b32_e32 v112, 16, v146
	v_and_b32_e32 v113, 0xffff0000, v146
	v_lshlrev_b32_e32 v114, 16, v147
	v_and_b32_e32 v115, 0xffff0000, v147
	v_pk_fma_f32 v[100:101], v[100:101], v[108:109], v[114:115]
	v_pk_fma_f32 v[98:99], v[98:99], v[106:107], v[112:113]
	s_nop 0
	v_cvt_pk_bf16_f32 v98, v98, v99
	v_cvt_pk_bf16_f32 v99, v100, v101
	v_cvt_pk_bf16_f32 v100, v102, v103
	v_cvt_pk_bf16_f32 v101, v104, v105
	global_store_dwordx4 v[110:111], v[98:101], off offset:256
	v_lshlrev_b32_e32 v102, 16, v152
	v_and_b32_e32 v103, 0xffff0000, v152
	v_lshlrev_b32_e32 v98, 16, v160
	v_and_b32_e32 v99, 0xffff0000, v160
	v_lshlrev_b32_e32 v100, 16, v161
	v_and_b32_e32 v101, 0xffff0000, v161
	v_lshlrev_b32_e32 v104, 16, v153
	v_and_b32_e32 v105, 0xffff0000, v153
	v_pk_fma_f32 v[96:97], v[96:97], v[100:101], v[104:105]
	v_pk_fma_f32 v[94:95], v[94:95], v[98:99], v[102:103]
	v_lshlrev_b32_e32 v98, 16, v158
	v_and_b32_e32 v99, 0xffff0000, v158
	v_lshlrev_b32_e32 v100, 16, v159
	v_and_b32_e32 v101, 0xffff0000, v159
	v_lshlrev_b32_e32 v102, 16, v150
	v_and_b32_e32 v103, 0xffff0000, v150
	v_lshlrev_b32_e32 v104, 16, v151
	v_and_b32_e32 v105, 0xffff0000, v151
	v_pk_fma_f32 v[92:93], v[92:93], v[100:101], v[104:105]
	v_pk_fma_f32 v[90:91], v[90:91], v[98:99], v[102:103]
	v_lshlrev_b32_e32 v98, 16, v133
	v_cvt_pk_bf16_f32 v90, v90, v91
	v_cvt_pk_bf16_f32 v91, v92, v93
	v_cvt_pk_bf16_f32 v92, v94, v95
	v_lshl_add_u64 v[94:95], s[18:19], 0, v[216:217]
	v_cvt_pk_bf16_f32 v93, v96, v97
	v_lshl_add_u64 v[94:95], v[94:95], 0, v[210:211]
	global_store_dwordx4 v[94:95], v[90:93], off
	v_lshlrev_b32_e32 v96, 16, v132
	v_and_b32_e32 v97, 0xffff0000, v132
	v_lshlrev_b32_e32 v90, 16, v136
	v_and_b32_e32 v91, 0xffff0000, v136
	v_lshlrev_b32_e32 v92, 16, v137
	v_and_b32_e32 v93, 0xffff0000, v137
	v_and_b32_e32 v99, 0xffff0000, v133
	v_pk_fma_f32 v[88:89], v[88:89], v[92:93], v[98:99]
	v_pk_fma_f32 v[86:87], v[86:87], v[90:91], v[96:97]
	v_lshlrev_b32_e32 v90, 16, v134
	v_and_b32_e32 v91, 0xffff0000, v134
	v_lshlrev_b32_e32 v92, 16, v135
	v_and_b32_e32 v93, 0xffff0000, v135
	v_lshlrev_b32_e32 v96, 16, v130
	v_and_b32_e32 v97, 0xffff0000, v130
	v_lshlrev_b32_e32 v98, 16, v131
	v_and_b32_e32 v99, 0xffff0000, v131
	v_pk_fma_f32 v[84:85], v[84:85], v[92:93], v[98:99]
	v_pk_fma_f32 v[82:83], v[82:83], v[90:91], v[96:97]
	s_nop 0
	v_cvt_pk_bf16_f32 v82, v82, v83
	v_cvt_pk_bf16_f32 v83, v84, v85
	v_cvt_pk_bf16_f32 v84, v86, v87
	v_cvt_pk_bf16_f32 v85, v88, v89
	global_store_dwordx4 v[94:95], v[82:85], off offset:256
	v_lshlrev_b32_e32 v86, 16, v164
	v_and_b32_e32 v87, 0xffff0000, v164
	v_lshlrev_b32_e32 v82, 16, v168
	v_and_b32_e32 v83, 0xffff0000, v168
	v_lshlrev_b32_e32 v84, 16, v169
	v_and_b32_e32 v85, 0xffff0000, v169
	v_lshlrev_b32_e32 v88, 16, v165
	v_and_b32_e32 v89, 0xffff0000, v165
	v_pk_fma_f32 v[80:81], v[80:81], v[84:85], v[88:89]
	v_pk_fma_f32 v[78:79], v[78:79], v[82:83], v[86:87]
	v_lshlrev_b32_e32 v82, 16, v166
	v_and_b32_e32 v83, 0xffff0000, v166
	v_lshlrev_b32_e32 v84, 16, v167
	v_and_b32_e32 v85, 0xffff0000, v167
	v_lshlrev_b32_e32 v86, 16, v162
	v_and_b32_e32 v87, 0xffff0000, v162
	v_lshlrev_b32_e32 v88, 16, v163
	v_and_b32_e32 v89, 0xffff0000, v163
	v_pk_fma_f32 v[76:77], v[76:77], v[84:85], v[88:89]
	v_pk_fma_f32 v[74:75], v[74:75], v[82:83], v[86:87]
	v_lshlrev_b32_e32 v82, 16, v141
	v_cvt_pk_bf16_f32 v74, v74, v75
	v_cvt_pk_bf16_f32 v75, v76, v77
	v_cvt_pk_bf16_f32 v76, v78, v79
	v_lshl_add_u64 v[78:79], s[18:19], 0, v[218:219]
	v_cvt_pk_bf16_f32 v77, v80, v81
	v_lshl_add_u64 v[78:79], v[78:79], 0, v[210:211]
	global_store_dwordx4 v[78:79], v[74:77], off
	v_lshlrev_b32_e32 v80, 16, v140
	v_and_b32_e32 v81, 0xffff0000, v140
	v_lshlrev_b32_e32 v74, 16, v144
	v_and_b32_e32 v75, 0xffff0000, v144
	v_lshlrev_b32_e32 v76, 16, v145
	v_and_b32_e32 v77, 0xffff0000, v145
	v_and_b32_e32 v83, 0xffff0000, v141
	v_pk_fma_f32 v[72:73], v[72:73], v[76:77], v[82:83]
	v_pk_fma_f32 v[70:71], v[70:71], v[74:75], v[80:81]
	v_lshlrev_b32_e32 v74, 16, v142
	v_and_b32_e32 v75, 0xffff0000, v142
	v_lshlrev_b32_e32 v76, 16, v143
	v_and_b32_e32 v77, 0xffff0000, v143
	v_lshlrev_b32_e32 v80, 16, v138
	v_and_b32_e32 v81, 0xffff0000, v138
	v_lshlrev_b32_e32 v82, 16, v139
	v_and_b32_e32 v83, 0xffff0000, v139
	v_pk_fma_f32 v[68:69], v[68:69], v[76:77], v[82:83]
	v_pk_fma_f32 v[66:67], v[66:67], v[74:75], v[80:81]
	s_nop 0
	v_cvt_pk_bf16_f32 v66, v66, v67
	v_cvt_pk_bf16_f32 v67, v68, v69
	v_cvt_pk_bf16_f32 v68, v70, v71
	v_cvt_pk_bf16_f32 v69, v72, v73
	global_store_dwordx4 v[78:79], v[66:69], off offset:256
	s_nop 1
	v_add_u32_e32 v66, 0x80, v212
	v_ashrrev_i32_e32 v67, 31, v66
	v_mad_i64_i32 v[68:69], s[14:15], v66, s26, v[214:215]
	v_lshlrev_b64 v[134:135], 12, v[66:67]
	v_lshl_add_u64 v[68:69], v[68:69], 0, v[210:211]
	v_lshl_add_u64 v[66:67], s[24:25], 0, v[134:135]
	global_load_dwordx4 v[102:105], v[68:69], off nt
	v_lshl_add_u64 v[66:67], v[66:67], 0, v[210:211]
; __device__ __forceinline__ unsigned cvt_pk_bf16(float lo, float hi) { f32x2_t v = {lo, hi}; bf16x2_t b = __builtin_convertvector(v, bf16x2_t); return __builtin_bit_cast(unsigned, b); }
;     __device__ __forceinline__ void operator()(const f32x4 (&acc)[2][2][4][2], const Unit& u, int wr, int wc, int fr, int fq) const {
;     ...
;                 for (int bj = 0; bj < 2; ++bj) { const int c = col0 + bj * HALF;
;                     gq[m][bj] = *(const u32x4*)(Z + row * ZLD + goff + c);
;                     if (u.be != 0) tq[m][bj] = *(const u32x4*)(tmp + row * D + c); } }
; #pragma unroll
;             for (int m = 0; m < 4; ++m) { const size_t row = (size_t)(row0 + ai * HALF + m * 16);
; #pragma unroll
;                 for (int bj = 0; bj < 2; ++bj) { const int c = col0 + bj * HALF; const u32x4 g = gq[m][bj];
;                     f32x4 v0 = acc[ai][bj][m][0] * (f32x4){bflo(g.x), bfhi(g.x), bflo(g.y), bfhi(g.y)};
;                     f32x4 v1 = acc[ai][bj][m][1] * (f32x4){bflo(g.z), bfhi(g.z), bflo(g.w), bfhi(g.w)};
;                     if (u.be != 0) { const u32x4 t = tq[m][bj];
;                         v0 = v0 + (f32x4){bflo(t.x), bfhi(t.x), bflo(t.y), bfhi(t.y)}; v1 = v1 + (f32x4){bflo(t.z), bfhi(t.z), bflo(t.w), bfhi(t.w)}; }
;                     u32x4 w; w.x = cvt_pk_bf16(v0[0], v0[1]); w.y = cvt_pk_bf16(v0[2], v0[3]); w.z = cvt_pk_bf16(v1[0], v1[1]); w.w = cvt_pk_bf16(v1[2], v1[3]);
;                     *(u32x4*)((u.be != 0 ? Y : tmp) + row * D + c) = w; } }
	global_load_dwordx4 v[106:109], v[66:67], off nt
	global_load_dwordx4 v[110:113], v[68:69], off offset:256 nt
	global_load_dwordx4 v[114:117], v[66:67], off offset:256 nt
	v_add_u32_e32 v66, 0x90, v212
	v_ashrrev_i32_e32 v67, 31, v66
	v_mad_i64_i32 v[68:69], s[14:15], v66, s26, v[214:215]
	v_lshlrev_b64 v[136:137], 12, v[66:67]
	v_lshl_add_u64 v[68:69], v[68:69], 0, v[210:211]
	v_lshl_add_u64 v[66:67], s[24:25], 0, v[136:137]
	global_load_dwordx4 v[118:121], v[68:69], off nt
	v_lshl_add_u64 v[66:67], v[66:67], 0, v[210:211]
	global_load_dwordx4 v[122:125], v[66:67], off nt
	global_load_dwordx4 v[126:129], v[68:69], off offset:256 nt
	global_load_dwordx4 v[130:133], v[66:67], off offset:256 nt
	v_add_u32_e32 v66, 0xa0, v212
	v_ashrrev_i32_e32 v67, 31, v66
	v_mad_i64_i32 v[68:69], s[14:15], v66, s26, v[214:215]
	v_lshlrev_b64 v[100:101], 12, v[66:67]
	v_lshl_add_u64 v[68:69], v[68:69], 0, v[210:211]
	v_lshl_add_u64 v[66:67], s[24:25], 0, v[100:101]
	global_load_dwordx4 v[90:93], v[68:69], off nt
	v_lshl_add_u64 v[66:67], v[66:67], 0, v[210:211]
	global_load_dwordx4 v[94:97], v[66:67], off nt
	global_load_dwordx4 v[82:85], v[68:69], off offset:256 nt
	global_load_dwordx4 v[86:89], v[66:67], off offset:256 nt
	v_add_u32_e32 v66, 0xb0, v212
	v_ashrrev_i32_e32 v67, 31, v66
	v_mad_i64_i32 v[68:69], s[14:15], v66, s26, v[214:215]
	v_lshlrev_b64 v[98:99], 12, v[66:67]
	v_lshl_add_u64 v[68:69], v[68:69], 0, v[210:211]
	v_lshl_add_u64 v[66:67], s[24:25], 0, v[98:99]
	global_load_dwordx4 v[74:77], v[68:69], off nt
	v_lshl_add_u64 v[70:71], v[66:67], 0, v[210:211]
	global_load_dwordx4 v[78:81], v[70:71], off nt
	s_nop 0
	global_load_dwordx4 v[66:69], v[68:69], off offset:256 nt
	s_nop 0
	global_load_dwordx4 v[70:73], v[70:71], off offset:256 nt
	s_waitcnt vmcnt(15)
	v_lshlrev_b32_e32 v138, 16, v104
	v_and_b32_e32 v139, 0xffff0000, v104
	v_lshlrev_b32_e32 v104, 16, v105
	v_and_b32_e32 v105, 0xffff0000, v105
	s_waitcnt vmcnt(14)
	v_lshlrev_b32_e32 v140, 16, v108
	v_and_b32_e32 v141, 0xffff0000, v108
	v_lshlrev_b32_e32 v108, 16, v109
	v_and_b32_e32 v109, 0xffff0000, v109
	v_pk_fma_f32 v[64:65], v[64:65], v[104:105], v[108:109]
	v_lshlrev_b32_e32 v104, 16, v102
	v_and_b32_e32 v105, 0xffff0000, v102
	v_lshlrev_b32_e32 v102, 16, v103
	v_and_b32_e32 v103, 0xffff0000, v103
	v_lshlrev_b32_e32 v108, 16, v106
	v_and_b32_e32 v109, 0xffff0000, v106
	v_lshlrev_b32_e32 v106, 16, v107
	v_and_b32_e32 v107, 0xffff0000, v107
	v_pk_fma_f32 v[62:63], v[62:63], v[138:139], v[140:141]
	v_pk_fma_f32 v[60:61], v[60:61], v[102:103], v[106:107]
	v_pk_fma_f32 v[58:59], v[58:59], v[104:105], v[108:109]
	s_waitcnt vmcnt(12)
	v_lshlrev_b32_e32 v102, 16, v117
	v_cvt_pk_bf16_f32 v58, v58, v59
	v_cvt_pk_bf16_f32 v59, v60, v61
	v_cvt_pk_bf16_f32 v60, v62, v63
	v_lshl_add_u64 v[62:63], s[18:19], 0, v[134:135]
	v_cvt_pk_bf16_f32 v61, v64, v65
	v_lshl_add_u64 v[62:63], v[62:63], 0, v[210:211]
	global_store_dwordx4 v[62:63], v[58:61], off
	v_lshlrev_b32_e32 v64, 16, v116
	v_and_b32_e32 v65, 0xffff0000, v116
	v_lshlrev_b32_e32 v58, 16, v112
	v_and_b32_e32 v59, 0xffff0000, v112
	v_lshlrev_b32_e32 v60, 16, v113
	v_and_b32_e32 v61, 0xffff0000, v113
	v_and_b32_e32 v103, 0xffff0000, v117
	v_pk_fma_f32 v[56:57], v[56:57], v[60:61], v[102:103]
	v_pk_fma_f32 v[54:55], v[54:55], v[58:59], v[64:65]
	v_lshlrev_b32_e32 v58, 16, v110
	v_and_b32_e32 v59, 0xffff0000, v110
	v_lshlrev_b32_e32 v60, 16, v111
	v_and_b32_e32 v61, 0xffff0000, v111
	v_lshlrev_b32_e32 v64, 16, v114
	v_and_b32_e32 v65, 0xffff0000, v114
	v_lshlrev_b32_e32 v102, 16, v115
	v_and_b32_e32 v103, 0xffff0000, v115
	v_pk_fma_f32 v[52:53], v[52:53], v[60:61], v[102:103]
	v_pk_fma_f32 v[50:51], v[50:51], v[58:59], v[64:65]
	s_nop 0
	v_cvt_pk_bf16_f32 v50, v50, v51
	v_cvt_pk_bf16_f32 v51, v52, v53
	v_cvt_pk_bf16_f32 v52, v54, v55
	v_cvt_pk_bf16_f32 v53, v56, v57
	global_store_dwordx4 v[62:63], v[50:53], off offset:256
	s_waitcnt vmcnt(12)
	v_lshlrev_b32_e32 v54, 16, v124
	v_and_b32_e32 v55, 0xffff0000, v124
	v_lshlrev_b32_e32 v50, 16, v120
	v_and_b32_e32 v51, 0xffff0000, v120
	v_lshlrev_b32_e32 v52, 16, v121
	v_and_b32_e32 v53, 0xffff0000, v121
	v_lshlrev_b32_e32 v56, 16, v125
	v_and_b32_e32 v57, 0xffff0000, v125
	v_pk_fma_f32 v[48:49], v[48:49], v[52:53], v[56:57]
	v_pk_fma_f32 v[46:47], v[46:47], v[50:51], v[54:55]
	v_lshlrev_b32_e32 v50, 16, v118
	v_and_b32_e32 v51, 0xffff0000, v118
	v_lshlrev_b32_e32 v52, 16, v119
	v_and_b32_e32 v53, 0xffff0000, v119
	v_lshlrev_b32_e32 v54, 16, v122
	v_and_b32_e32 v55, 0xffff0000, v122
	v_lshlrev_b32_e32 v56, 16, v123
	v_and_b32_e32 v57, 0xffff0000, v123
	v_pk_fma_f32 v[44:45], v[44:45], v[52:53], v[56:57]
	v_pk_fma_f32 v[42:43], v[42:43], v[50:51], v[54:55]
	s_waitcnt vmcnt(10)
; __device__ __forceinline__ unsigned cvt_pk_bf16(float lo, float hi) { f32x2_t v = {lo, hi}; bf16x2_t b = __builtin_convertvector(v, bf16x2_t); return __builtin_bit_cast(unsigned, b); }
;     __device__ __forceinline__ void operator()(const f32x4 (&acc)[2][2][4][2], const Unit& u, int wr, int wc, int fr, int fq) const {
;     ...
;             for (int m = 0; m < 4; ++m) { const size_t row = (size_t)(row0 + ai * HALF + m * 16);
; #pragma unroll
;                 for (int bj = 0; bj < 2; ++bj) { const int c = col0 + bj * HALF; const u32x4 g = gq[m][bj];
;                     f32x4 v0 = acc[ai][bj][m][0] * (f32x4){bflo(g.x), bfhi(g.x), bflo(g.y), bfhi(g.y)};
;                     f32x4 v1 = acc[ai][bj][m][1] * (f32x4){bflo(g.z), bfhi(g.z), bflo(g.w), bfhi(g.w)};
;                     if (u.be != 0) { const u32x4 t = tq[m][bj];
;                         v0 = v0 + (f32x4){bflo(t.x), bfhi(t.x), bflo(t.y), bfhi(t.y)}; v1 = v1 + (f32x4){bflo(t.z), bfhi(t.z), bflo(t.w), bfhi(t.w)}; }
;                     u32x4 w; w.x = cvt_pk_bf16(v0[0], v0[1]); w.y = cvt_pk_bf16(v0[2], v0[3]); w.z = cvt_pk_bf16(v1[0], v1[1]); w.w = cvt_pk_bf16(v1[2], v1[3]);
;                     *(u32x4*)((u.be != 0 ? Y : tmp) + row * D + c) = w; } }
	v_lshlrev_b32_e32 v50, 16, v133
	v_cvt_pk_bf16_f32 v42, v42, v43
	v_cvt_pk_bf16_f32 v43, v44, v45
	v_cvt_pk_bf16_f32 v44, v46, v47
	v_lshl_add_u64 v[46:47], s[18:19], 0, v[136:137]
	v_cvt_pk_bf16_f32 v45, v48, v49
	v_lshl_add_u64 v[46:47], v[46:47], 0, v[210:211]
	global_store_dwordx4 v[46:47], v[42:45], off
	v_lshlrev_b32_e32 v48, 16, v132
	v_and_b32_e32 v49, 0xffff0000, v132
	v_lshlrev_b32_e32 v42, 16, v128
	v_and_b32_e32 v43, 0xffff0000, v128
	v_lshlrev_b32_e32 v44, 16, v129
	v_and_b32_e32 v45, 0xffff0000, v129
	v_and_b32_e32 v51, 0xffff0000, v133
	v_pk_fma_f32 v[40:41], v[40:41], v[44:45], v[50:51]
	v_pk_fma_f32 v[38:39], v[38:39], v[42:43], v[48:49]
	v_lshlrev_b32_e32 v42, 16, v126
	v_and_b32_e32 v43, 0xffff0000, v126
	v_lshlrev_b32_e32 v44, 16, v127
	v_and_b32_e32 v45, 0xffff0000, v127
	v_lshlrev_b32_e32 v48, 16, v130
	v_and_b32_e32 v49, 0xffff0000, v130
	v_lshlrev_b32_e32 v50, 16, v131
	v_and_b32_e32 v51, 0xffff0000, v131
	v_pk_fma_f32 v[36:37], v[36:37], v[44:45], v[50:51]
	v_pk_fma_f32 v[34:35], v[34:35], v[42:43], v[48:49]
	s_nop 0
	v_cvt_pk_bf16_f32 v34, v34, v35
	v_cvt_pk_bf16_f32 v35, v36, v37
	v_cvt_pk_bf16_f32 v36, v38, v39
	v_cvt_pk_bf16_f32 v37, v40, v41
	global_store_dwordx4 v[46:47], v[34:37], off offset:256
	s_waitcnt vmcnt(10)
	v_lshlrev_b32_e32 v38, 16, v96
	v_and_b32_e32 v39, 0xffff0000, v96
	v_lshlrev_b32_e32 v34, 16, v92
	v_and_b32_e32 v35, 0xffff0000, v92
	v_lshlrev_b32_e32 v36, 16, v93
	v_and_b32_e32 v37, 0xffff0000, v93
	v_lshlrev_b32_e32 v40, 16, v97
	v_and_b32_e32 v41, 0xffff0000, v97
	v_pk_fma_f32 v[32:33], v[32:33], v[36:37], v[40:41]
	v_pk_fma_f32 v[30:31], v[30:31], v[34:35], v[38:39]
	v_lshlrev_b32_e32 v34, 16, v90
	v_and_b32_e32 v35, 0xffff0000, v90
	v_lshlrev_b32_e32 v36, 16, v91
	v_and_b32_e32 v37, 0xffff0000, v91
	v_lshlrev_b32_e32 v38, 16, v94
	v_and_b32_e32 v39, 0xffff0000, v94
	v_lshlrev_b32_e32 v40, 16, v95
	v_and_b32_e32 v41, 0xffff0000, v95
	v_pk_fma_f32 v[28:29], v[28:29], v[36:37], v[40:41]
	v_pk_fma_f32 v[26:27], v[26:27], v[34:35], v[38:39]
	s_waitcnt vmcnt(8)
	v_lshlrev_b32_e32 v34, 16, v89
	v_cvt_pk_bf16_f32 v26, v26, v27
	v_cvt_pk_bf16_f32 v27, v28, v29
	v_cvt_pk_bf16_f32 v28, v30, v31
	v_lshl_add_u64 v[30:31], s[18:19], 0, v[100:101]
	v_cvt_pk_bf16_f32 v29, v32, v33
	v_lshl_add_u64 v[30:31], v[30:31], 0, v[210:211]
	global_store_dwordx4 v[30:31], v[26:29], off
	v_lshlrev_b32_e32 v32, 16, v88
	v_and_b32_e32 v33, 0xffff0000, v88
	v_lshlrev_b32_e32 v26, 16, v84
	v_and_b32_e32 v27, 0xffff0000, v84
	v_lshlrev_b32_e32 v28, 16, v85
	v_and_b32_e32 v29, 0xffff0000, v85
	v_and_b32_e32 v35, 0xffff0000, v89
	v_pk_fma_f32 v[24:25], v[24:25], v[28:29], v[34:35]
	v_pk_fma_f32 v[22:23], v[22:23], v[26:27], v[32:33]
	v_lshlrev_b32_e32 v26, 16, v82
	v_and_b32_e32 v27, 0xffff0000, v82
	v_lshlrev_b32_e32 v28, 16, v83
	v_and_b32_e32 v29, 0xffff0000, v83
	v_lshlrev_b32_e32 v32, 16, v86
	v_and_b32_e32 v33, 0xffff0000, v86
	v_lshlrev_b32_e32 v34, 16, v87
	v_and_b32_e32 v35, 0xffff0000, v87
	v_pk_fma_f32 v[20:21], v[20:21], v[28:29], v[34:35]
	v_pk_fma_f32 v[18:19], v[18:19], v[26:27], v[32:33]
	s_nop 0
	v_cvt_pk_bf16_f32 v18, v18, v19
	v_cvt_pk_bf16_f32 v19, v20, v21
	v_cvt_pk_bf16_f32 v20, v22, v23
	v_cvt_pk_bf16_f32 v21, v24, v25
	global_store_dwordx4 v[30:31], v[18:21], off offset:256
	s_waitcnt vmcnt(8)
	v_lshlrev_b32_e32 v22, 16, v80
	v_and_b32_e32 v23, 0xffff0000, v80
	v_lshlrev_b32_e32 v18, 16, v76
	v_and_b32_e32 v19, 0xffff0000, v76
	v_lshlrev_b32_e32 v20, 16, v77
	v_and_b32_e32 v21, 0xffff0000, v77
	v_lshlrev_b32_e32 v24, 16, v81
	v_and_b32_e32 v25, 0xffff0000, v81
	v_pk_fma_f32 v[16:17], v[16:17], v[20:21], v[24:25]
	v_pk_fma_f32 v[14:15], v[14:15], v[18:19], v[22:23]
	v_lshlrev_b32_e32 v18, 16, v74
	v_and_b32_e32 v19, 0xffff0000, v74
	v_lshlrev_b32_e32 v20, 16, v75
	v_and_b32_e32 v21, 0xffff0000, v75
	v_lshlrev_b32_e32 v22, 16, v78
	v_and_b32_e32 v23, 0xffff0000, v78
	v_lshlrev_b32_e32 v24, 16, v79
	v_and_b32_e32 v25, 0xffff0000, v79
	v_pk_fma_f32 v[12:13], v[12:13], v[20:21], v[24:25]
	v_pk_fma_f32 v[10:11], v[10:11], v[18:19], v[22:23]
	s_waitcnt vmcnt(6)
	v_lshlrev_b32_e32 v18, 16, v73
	v_cvt_pk_bf16_f32 v10, v10, v11
	v_cvt_pk_bf16_f32 v11, v12, v13
	v_cvt_pk_bf16_f32 v12, v14, v15
	v_lshl_add_u64 v[14:15], s[18:19], 0, v[98:99]
	v_cvt_pk_bf16_f32 v13, v16, v17
	v_lshl_add_u64 v[14:15], v[14:15], 0, v[210:211]
	global_store_dwordx4 v[14:15], v[10:13], off
	v_lshlrev_b32_e32 v16, 16, v72
	v_and_b32_e32 v17, 0xffff0000, v72
	v_lshlrev_b32_e32 v10, 16, v68
	v_and_b32_e32 v11, 0xffff0000, v68
	v_lshlrev_b32_e32 v12, 16, v69
	v_and_b32_e32 v13, 0xffff0000, v69
	v_and_b32_e32 v19, 0xffff0000, v73
	v_pk_fma_f32 v[8:9], v[8:9], v[12:13], v[18:19]
	v_pk_fma_f32 v[6:7], v[6:7], v[10:11], v[16:17]
	v_lshlrev_b32_e32 v10, 16, v66
	v_and_b32_e32 v11, 0xffff0000, v66
	v_lshlrev_b32_e32 v12, 16, v67
	v_and_b32_e32 v13, 0xffff0000, v67
	v_lshlrev_b32_e32 v16, 16, v70
	v_and_b32_e32 v17, 0xffff0000, v70
	v_lshlrev_b32_e32 v18, 16, v71
	v_and_b32_e32 v19, 0xffff0000, v71
	v_pk_fma_f32 v[4:5], v[4:5], v[12:13], v[18:19]
	v_pk_fma_f32 v[2:3], v[2:3], v[10:11], v[16:17]
	s_mov_b64 s[18:19], -1
	v_cvt_pk_bf16_f32 v2, v2, v3
	v_cvt_pk_bf16_f32 v3, v4, v5
	v_cvt_pk_bf16_f32 v4, v6, v7
	v_cvt_pk_bf16_f32 v5, v8, v9
	global_store_dwordx4 v[14:15], v[2:5], off offset:256
	s_cbranch_vccnz .LBB0_610
	s_andn2_b64 vcc, exec, s[4:5]
	s_cbranch_vccnz .LBB0_609
	s_barrier
	s_branch .LBB0_609

;     __device__ __forceinline__ void operator()(const f32x4 (&acc)[2][2][4][2], const Unit& u, int wr, int wc, int fr, int fq) const {
;         const int row0 = u.pm * BM + wr * 64 + fr, col0 = u.pn * BM + wc * 32 + 4 * fq;
; #pragma unroll
;         for (int ai = 0; ai < 2; ++ai) {
;             f32x4 bs[4][2][2];
; #pragma unroll
;             for (int m = 0; m < 4; ++m) { const size_t off = (size_t)(row0 + ai * HALF + m * 16) * D + col0;
; #pragma unroll
;                 for (int bj = 0; bj < 2; ++bj)
; #pragma unroll
;                     for (int n = 0; n < 2; ++n) bs[m][bj][n] = *(const f32x4*)(base + off + bj * HALF + n * 16); }
; #pragma unroll
;             for (int m = 0; m < 4; ++m) { const size_t off = (size_t)(row0 + ai * HALF + m * 16) * D + col0;
; #pragma unroll
;                 for (int bj = 0; bj < 2; ++bj)
; #pragma unroll
;                     for (int n = 0; n < 2; ++n) *(f32x4*)(out + off + bj * HALF + n * 16) = bs[m][bj][n] + acc[ai][bj][m][n]; }
;         }
.LBB0_694:
	v_lshl_or_b32 v132, s50, 8, v157
	v_lshl_add_u32 v130, s51, 8, v1
	v_ashrrev_i32_e32 v133, 31, v132
	v_lshlrev_b64 v[148:149], 2, v[132:133]
	v_ashrrev_i32_e32 v131, 31, v130
	v_lshl_add_u64 v[150:151], s[6:7], 0, v[148:149]
	v_lshlrev_b64 v[152:153], 13, v[130:131]
	v_lshl_add_u64 v[132:133], v[150:151], 0, v[152:153]
	global_load_dwordx4 v[160:163], v[132:133], off nt
	global_load_dwordx4 v[164:167], v[132:133], off offset:64 nt
	global_load_dwordx4 v[168:171], v[132:133], off offset:512 nt
	global_load_dwordx4 v[172:175], v[132:133], off offset:576 nt
	v_or_b32_e32 v132, 16, v130
	v_ashrrev_i32_e32 v133, 31, v132
	v_lshlrev_b64 v[184:185], 13, v[132:133]
	v_lshl_add_u64 v[132:133], v[150:151], 0, v[184:185]
	global_load_dwordx4 v[176:179], v[132:133], off nt
	global_load_dwordx4 v[180:183], v[132:133], off offset:64 nt
	global_load_dwordx4 v[200:203], v[132:133], off offset:512 nt
	global_load_dwordx4 v[204:207], v[132:133], off offset:576 nt
	v_or_b32_e32 v132, 32, v130
	v_ashrrev_i32_e32 v133, 31, v132
	v_or_b32_e32 v130, 48, v130
	v_lshlrev_b64 v[236:237], 13, v[132:133]
	v_ashrrev_i32_e32 v131, 31, v130
	v_lshl_add_u64 v[132:133], v[150:151], 0, v[236:237]
	v_lshlrev_b64 v[154:155], 13, v[130:131]
	global_load_dwordx4 v[208:211], v[132:133], off nt
	global_load_dwordx4 v[212:215], v[132:133], off offset:64 nt
	global_load_dwordx4 v[216:219], v[132:133], off offset:512 nt
	global_load_dwordx4 v[220:223], v[132:133], off offset:576 nt
	v_lshl_add_u64 v[130:131], v[150:151], 0, v[154:155]
	global_load_dwordx4 v[232:235], v[130:131], off nt
	global_load_dwordx4 v[138:141], v[130:131], off offset:64 nt
	global_load_dwordx4 v[134:137], v[130:131], off offset:512 nt
	s_nop 0
	global_load_dwordx4 v[130:133], v[130:131], off offset:576 nt
	s_mov_b64 s[14:15], 0x100000
	s_mov_b64 s[20:21], -1
	s_andn2_b64 vcc, exec, s[0:1]
	s_waitcnt vmcnt(0)
	v_pk_add_f32 v[126:127], v[126:127], v[160:161]
	v_lshl_add_u64 v[160:161], s[2:3], 0, v[152:153]
	v_lshl_add_u64 v[160:161], v[160:161], 0, v[148:149]
	v_pk_add_f32 v[116:117], v[116:117], v[170:171]
	v_pk_add_f32 v[114:115], v[114:115], v[168:169]
	global_store_dwordx4 v[160:161], v[114:117], off offset:512
	v_pk_add_f32 v[112:113], v[112:113], v[174:175]
	v_pk_add_f32 v[100:101], v[100:101], v[202:203]
	v_lshl_add_u64 v[114:115], s[2:3], 0, v[184:185]
	v_lshl_add_u64 v[114:115], v[114:115], 0, v[148:149]
	v_pk_add_f32 v[98:99], v[98:99], v[200:201]
	global_store_dwordx4 v[114:115], v[98:101], off offset:512
	v_pk_add_f32 v[110:111], v[110:111], v[172:173]
	v_pk_add_f32 v[96:97], v[96:97], v[206:207]
	v_lshl_add_u64 v[98:99], s[2:3], 0, v[236:237]
	v_lshl_add_u64 v[98:99], v[98:99], 0, v[148:149]
	v_pk_add_f32 v[84:85], v[84:85], v[218:219]
	v_pk_add_f32 v[82:83], v[82:83], v[216:217]
	v_pk_add_f32 v[94:95], v[94:95], v[204:205]
	global_store_dwordx4 v[98:99], v[82:85], off offset:512
	v_pk_add_f32 v[80:81], v[80:81], v[222:223]
	v_pk_add_f32 v[78:79], v[78:79], v[220:221]
	v_lshl_add_u64 v[82:83], s[2:3], 0, v[154:155]
	v_pk_add_f32 v[128:129], v[128:129], v[162:163]
	v_pk_add_f32 v[124:125], v[124:125], v[166:167]
	v_pk_add_f32 v[122:123], v[122:123], v[164:165]
	global_store_dwordx4 v[160:161], v[110:113], off offset:576
	v_pk_add_f32 v[108:109], v[108:109], v[182:183]
	v_pk_add_f32 v[106:107], v[106:107], v[180:181]
	v_pk_add_f32 v[112:113], v[120:121], v[178:179]
	v_pk_add_f32 v[110:111], v[118:119], v[176:177]
	global_store_dwordx4 v[114:115], v[94:97], off offset:576
	v_pk_add_f32 v[92:93], v[92:93], v[214:215]
	v_pk_add_f32 v[90:91], v[90:91], v[212:213]
	v_pk_add_f32 v[96:97], v[104:105], v[210:211]
	v_pk_add_f32 v[94:95], v[102:103], v[208:209]
	global_store_dwordx4 v[98:99], v[78:81], off offset:576
	v_lshl_add_u64 v[82:83], v[82:83], 0, v[148:149]
	v_pk_add_f32 v[76:77], v[76:77], v[140:141]
	v_pk_add_f32 v[80:81], v[88:89], v[234:235]
	v_pk_add_f32 v[78:79], v[86:87], v[232:233]
	v_pk_add_f32 v[74:75], v[74:75], v[138:139]
	v_pk_add_f32 v[72:73], v[72:73], v[136:137]
	v_pk_add_f32 v[70:71], v[70:71], v[134:135]
	v_pk_add_f32 v[68:69], v[68:69], v[132:133]
	v_pk_add_f32 v[66:67], v[66:67], v[130:131]
	v_lshl_add_u64 v[132:133], v[152:153], 0, s[14:15]
	global_store_dwordx4 v[160:161], v[126:129], off
	global_store_dwordx4 v[160:161], v[122:125], off offset:64
	global_store_dwordx4 v[114:115], v[110:113], off
	global_store_dwordx4 v[114:115], v[106:109], off offset:64
	global_store_dwordx4 v[98:99], v[94:97], off
	global_store_dwordx4 v[98:99], v[90:93], off offset:64
	global_store_dwordx4 v[82:83], v[78:81], off
	global_store_dwordx4 v[82:83], v[74:77], off offset:64
	global_store_dwordx4 v[82:83], v[70:73], off offset:512
	global_store_dwordx4 v[82:83], v[66:69], off offset:576
	s_mov_b64 s[14:15], 0x120000
	v_lshl_add_u64 v[134:135], v[152:153], 0, s[14:15]
	v_lshl_add_u64 v[66:67], v[150:151], 0, v[132:133]
	global_load_dwordx4 v[80:83], v[66:67], off nt
	global_load_dwordx4 v[84:87], v[66:67], off offset:64 nt
	global_load_dwordx4 v[88:91], v[66:67], off offset:512 nt
	global_load_dwordx4 v[92:95], v[66:67], off offset:576 nt
	v_lshl_add_u64 v[66:67], v[150:151], 0, v[134:135]
	s_mov_b64 s[14:15], 0x140000
	global_load_dwordx4 v[96:99], v[66:67], off nt
	global_load_dwordx4 v[100:103], v[66:67], off offset:64 nt
	global_load_dwordx4 v[104:107], v[66:67], off offset:512 nt
	global_load_dwordx4 v[108:111], v[66:67], off offset:576 nt
	v_lshl_add_u64 v[136:137], v[152:153], 0, s[14:15]
	s_mov_b64 s[14:15], 0x160000
	v_lshl_add_u64 v[66:67], v[150:151], 0, v[136:137]
	v_lshl_add_u64 v[78:79], v[152:153], 0, s[14:15]
	global_load_dwordx4 v[112:115], v[66:67], off nt
	global_load_dwordx4 v[116:119], v[66:67], off offset:64 nt
	global_load_dwordx4 v[120:123], v[66:67], off offset:512 nt
	global_load_dwordx4 v[124:127], v[66:67], off offset:576 nt
	v_lshl_add_u64 v[66:67], v[150:151], 0, v[78:79]
	global_load_dwordx4 v[128:131], v[66:67], off nt
	global_load_dwordx4 v[74:77], v[66:67], off offset:64 nt
	global_load_dwordx4 v[70:73], v[66:67], off offset:512 nt
	s_nop 0
	global_load_dwordx4 v[66:69], v[66:67], off offset:576 nt
	s_waitcnt vmcnt(15)
;     __device__ __forceinline__ void operator()(const f32x4 (&acc)[2][2][4][2], const Unit& u, int wr, int wc, int fr, int fq) const {
;     ...
; #pragma unroll
;             for (int m = 0; m < 4; ++m) { const size_t off = (size_t)(row0 + ai * HALF + m * 16) * D + col0;
; #pragma unroll
;                 for (int bj = 0; bj < 2; ++bj)
; #pragma unroll
;                     for (int n = 0; n < 2; ++n) *(f32x4*)(out + off + bj * HALF + n * 16) = bs[m][bj][n] + acc[ai][bj][m][n]; }
;         }
	v_pk_add_f32 v[62:63], v[62:63], v[80:81]
	v_lshl_add_u64 v[80:81], s[2:3], 0, v[132:133]
	v_lshl_add_u64 v[80:81], v[80:81], 0, v[148:149]
	s_waitcnt vmcnt(13)
	v_pk_add_f32 v[52:53], v[52:53], v[90:91]
	v_pk_add_f32 v[50:51], v[50:51], v[88:89]
	global_store_dwordx4 v[80:81], v[50:53], off offset:512
	s_waitcnt vmcnt(10)
	v_pk_add_f32 v[36:37], v[36:37], v[106:107]
	v_pk_add_f32 v[34:35], v[34:35], v[104:105]
	v_lshl_add_u64 v[50:51], s[2:3], 0, v[134:135]
	v_lshl_add_u64 v[50:51], v[50:51], 0, v[148:149]
	global_store_dwordx4 v[50:51], v[34:37], off offset:512
	s_waitcnt vmcnt(7)
	v_pk_add_f32 v[20:21], v[20:21], v[122:123]
	v_pk_add_f32 v[18:19], v[18:19], v[120:121]
	v_lshl_add_u64 v[34:35], s[2:3], 0, v[136:137]
	v_lshl_add_u64 v[34:35], v[34:35], 0, v[148:149]
	v_pk_add_f32 v[48:49], v[48:49], v[94:95]
	v_pk_add_f32 v[46:47], v[46:47], v[92:93]
	v_pk_add_f32 v[32:33], v[32:33], v[110:111]
	v_pk_add_f32 v[30:31], v[30:31], v[108:109]
	global_store_dwordx4 v[34:35], v[18:21], off offset:512
	s_waitcnt vmcnt(7)
	v_pk_add_f32 v[16:17], v[16:17], v[126:127]
	v_pk_add_f32 v[14:15], v[14:15], v[124:125]
	v_lshl_add_u64 v[18:19], s[2:3], 0, v[78:79]
	v_pk_add_f32 v[64:65], v[64:65], v[82:83]
	v_pk_add_f32 v[60:61], v[60:61], v[86:87]
	v_pk_add_f32 v[58:59], v[58:59], v[84:85]
	global_store_dwordx4 v[80:81], v[46:49], off offset:576
	v_pk_add_f32 v[44:45], v[44:45], v[102:103]
	v_pk_add_f32 v[42:43], v[42:43], v[100:101]
	v_pk_add_f32 v[48:49], v[56:57], v[98:99]
	v_pk_add_f32 v[46:47], v[54:55], v[96:97]
	global_store_dwordx4 v[50:51], v[30:33], off offset:576
	v_pk_add_f32 v[28:29], v[28:29], v[118:119]
	v_pk_add_f32 v[26:27], v[26:27], v[116:117]
	v_pk_add_f32 v[32:33], v[40:41], v[114:115]
	v_pk_add_f32 v[30:31], v[38:39], v[112:113]
	global_store_dwordx4 v[34:35], v[14:17], off offset:576
	v_lshl_add_u64 v[18:19], v[18:19], 0, v[148:149]
	s_waitcnt vmcnt(8)
	v_pk_add_f32 v[12:13], v[12:13], v[76:77]
	v_pk_add_f32 v[16:17], v[24:25], v[130:131]
	v_pk_add_f32 v[14:15], v[22:23], v[128:129]
	v_pk_add_f32 v[10:11], v[10:11], v[74:75]
	s_waitcnt vmcnt(7)
	v_pk_add_f32 v[8:9], v[8:9], v[72:73]
	v_pk_add_f32 v[6:7], v[6:7], v[70:71]
	s_waitcnt vmcnt(6)
	v_pk_add_f32 v[4:5], v[4:5], v[68:69]
	v_pk_add_f32 v[2:3], v[2:3], v[66:67]
	global_store_dwordx4 v[80:81], v[62:65], off
	global_store_dwordx4 v[80:81], v[58:61], off offset:64
	global_store_dwordx4 v[50:51], v[46:49], off
	global_store_dwordx4 v[50:51], v[42:45], off offset:64
	global_store_dwordx4 v[34:35], v[30:33], off
	global_store_dwordx4 v[34:35], v[26:29], off offset:64
	global_store_dwordx4 v[18:19], v[14:17], off
	global_store_dwordx4 v[18:19], v[10:13], off offset:64
	global_store_dwordx4 v[18:19], v[6:9], off offset:512
	global_store_dwordx4 v[18:19], v[2:5], off offset:576
	s_cbranch_vccnz .LBB0_683
	s_andn2_b64 vcc, exec, s[4:5]
	s_cbranch_vccnz .LBB0_682
	s_barrier
	s_branch .LBB0_682

; __global__ void __launch_bounds__(NWAVES * 64, 2) trunk_fwd(Args args) {
;     ...
;             for (int q = 2 * wave; q < npair; q += 2 * NWAVES) { const int m = r0 + (q >> 1);
;                 const v4u* src = (const v4u*)(Hb + (size_t)m * D); v4u* d0 = (v4u*)(HPERM + (size_t)SH[320 + q] * D); v4u* d1 = (v4u*)(HPERM + (size_t)SH[320 + q + 1] * D);
;                 v4u t[4];
; #pragma unroll
;                 for (int jj = 0; jj < 4; ++jj) t[jj] = src[lane + 64 * jj];
; #pragma unroll
;                 for (int jj = 0; jj < 4; ++jj) { d0[lane + 64 * jj] = t[jj]; d1[lane + 64 * jj] = t[jj]; } }
.LBB0_980:
	s_ashr_i32 s4, s0, 1
	s_add_i32 s4, s4, s6
	s_ashr_i32 s5, s4, 31
	s_lshl_b64 s[4:5], s[4:5], 12
	v_lshl_add_u64 v[18:19], v[2:3], 0, s[4:5]
	global_load_dwordx4 v[6:9], v[18:19], off nt
	global_load_dwordx4 v[10:13], v[18:19], off offset:1024 nt
	global_load_dwordx4 v[14:17], v[18:19], off offset:2048 nt
	s_nop 0
	global_load_dwordx4 v[18:21], v[18:19], off offset:3072 nt
	v_mov_b32_e32 v1, s1
	ds_read_b64 v[22:23], v1
	s_add_i32 s0, s0, 16
	s_add_i32 s1, s1, 64
	s_cmp_ge_i32 s0, s7
	s_waitcnt lgkmcnt(0)
	v_ashrrev_i32_e32 v25, 31, v22
	v_mov_b32_e32 v24, v22
	v_ashrrev_i32_e32 v27, 31, v23
	v_mov_b32_e32 v26, v23
	v_lshlrev_b64 v[24:25], 12, v[24:25]
	v_lshlrev_b64 v[22:23], 12, v[26:27]
	v_lshl_add_u64 v[24:25], v[4:5], 0, v[24:25]
	v_lshl_add_u64 v[22:23], v[4:5], 0, v[22:23]
	s_waitcnt vmcnt(3)
	global_store_dwordx4 v[24:25], v[6:9], off
	global_store_dwordx4 v[22:23], v[6:9], off
	s_waitcnt vmcnt(4)
	global_store_dwordx4 v[24:25], v[10:13], off offset:1024
	global_store_dwordx4 v[22:23], v[10:13], off offset:1024
	s_waitcnt vmcnt(5)
	global_store_dwordx4 v[24:25], v[14:17], off offset:2048
	global_store_dwordx4 v[22:23], v[14:17], off offset:2048
	s_waitcnt vmcnt(6)
	global_store_dwordx4 v[24:25], v[18:21], off offset:3072
	global_store_dwordx4 v[22:23], v[18:21], off offset:3072
	s_cbranch_scc0 .LBB0_980

;     __device__ __forceinline__ void operator()(const f32x4 (&acc)[2][2][4][2], const Unit& u, int wr, int wc, int fr, int fq) const {
;         const int row0 = u.pm * BM + wr * 64 + fr, col0 = u.pn * BM + wc * 32 + 4 * fq;
; #pragma unroll
;         for (int ai = 0; ai < 2; ++ai) {
;             f32x4 bs[4][2][2];
; #pragma unroll
;             for (int m = 0; m < 4; ++m) { const size_t off = (size_t)(row0 + ai * HALF + m * 16) * D + col0;
; #pragma unroll
;                 for (int bj = 0; bj < 2; ++bj)
; #pragma unroll
;                     for (int n = 0; n < 2; ++n) bs[m][bj][n] = *(const f32x4*)(base + off + bj * HALF + n * 16); }
; #pragma unroll
;             for (int m = 0; m < 4; ++m) { const size_t off = (size_t)(row0 + ai * HALF + m * 16) * D + col0;
; #pragma unroll
;                 for (int bj = 0; bj < 2; ++bj)
; #pragma unroll
;                     for (int n = 0; n < 2; ++n) *(f32x4*)(out + off + bj * HALF + n * 16) = bs[m][bj][n] + acc[ai][bj][m][n]; }
;         }
.LBB0_1291:
	v_lshl_or_b32 v136, s46, 8, v149
	v_lshl_add_u32 v146, s47, 8, v1
	v_ashrrev_i32_e32 v137, 31, v136
	v_lshlrev_b64 v[136:137], 2, v[136:137]
	v_ashrrev_i32_e32 v147, 31, v146
	v_lshl_add_u64 v[138:139], s[2:3], 0, v[136:137]
	v_lshlrev_b64 v[140:141], 13, v[146:147]
	v_or_b32_e32 v164, 16, v146
	v_lshl_add_u64 v[160:161], v[138:139], 0, v[140:141]
	v_ashrrev_i32_e32 v165, 31, v164
	global_load_dwordx4 v[142:145], v[160:161], off nt
	global_load_dwordx4 v[152:155], v[160:161], off offset:64 nt
	global_load_dwordx4 v[156:159], v[160:161], off offset:512 nt
	s_nop 0
	global_load_dwordx4 v[160:163], v[160:161], off offset:576 nt
	v_lshlrev_b64 v[184:185], 13, v[164:165]
	v_or_b32_e32 v180, 32, v146
	v_lshl_add_u64 v[176:177], v[138:139], 0, v[184:185]
	v_ashrrev_i32_e32 v181, 31, v180
	global_load_dwordx4 v[164:167], v[176:177], off nt
	global_load_dwordx4 v[168:171], v[176:177], off offset:64 nt
	global_load_dwordx4 v[172:175], v[176:177], off offset:512 nt
	s_nop 0
	global_load_dwordx4 v[176:179], v[176:177], off offset:576 nt
	v_lshlrev_b64 v[236:237], 13, v[180:181]
	v_or_b32_e32 v146, 48, v146
	v_lshl_add_u64 v[208:209], v[138:139], 0, v[236:237]
	v_ashrrev_i32_e32 v147, 31, v146
	global_load_dwordx4 v[180:183], v[208:209], off nt
	global_load_dwordx4 v[200:203], v[208:209], off offset:64 nt
	global_load_dwordx4 v[204:207], v[208:209], off offset:512 nt
	s_nop 0
	global_load_dwordx4 v[208:211], v[208:209], off offset:576 nt
	v_lshlrev_b64 v[146:147], 13, v[146:147]
	v_lshl_add_u64 v[232:233], v[138:139], 0, v[146:147]
	global_load_dwordx4 v[212:215], v[232:233], off nt
	global_load_dwordx4 v[216:219], v[232:233], off offset:64 nt
	global_load_dwordx4 v[220:223], v[232:233], off offset:512 nt
	s_nop 0
	global_load_dwordx4 v[232:235], v[232:233], off offset:576 nt
	s_mov_b64 s[12:13], 0x100000
	s_and_b64 vcc, exec, s[0:1]
	s_waitcnt vmcnt(0)
	v_pk_add_f32 v[126:127], v[126:127], v[142:143]
	v_lshl_add_u64 v[142:143], s[2:3], 0, v[140:141]
	v_lshl_add_u64 v[142:143], v[142:143], 0, v[136:137]
	v_pk_add_f32 v[112:113], v[112:113], v[158:159]
	v_pk_add_f32 v[110:111], v[110:111], v[156:157]
	global_store_dwordx4 v[142:143], v[110:113], off offset:512
	v_pk_add_f32 v[104:105], v[104:105], v[162:163]
	v_pk_add_f32 v[96:97], v[96:97], v[174:175]
	v_lshl_add_u64 v[110:111], s[2:3], 0, v[184:185]
	v_lshl_add_u64 v[110:111], v[110:111], 0, v[136:137]
	v_pk_add_f32 v[94:95], v[94:95], v[172:173]
	global_store_dwordx4 v[110:111], v[94:97], off offset:512
	v_pk_add_f32 v[80:81], v[80:81], v[206:207]
	v_pk_add_f32 v[78:79], v[78:79], v[204:205]
	v_lshl_add_u64 v[94:95], s[2:3], 0, v[236:237]
	v_lshl_add_u64 v[94:95], v[94:95], 0, v[136:137]
	v_pk_add_f32 v[102:103], v[102:103], v[160:161]
	v_pk_add_f32 v[88:89], v[88:89], v[178:179]
	v_pk_add_f32 v[86:87], v[86:87], v[176:177]
	global_store_dwordx4 v[94:95], v[78:81], off offset:512
	v_pk_add_f32 v[76:77], v[76:77], v[210:211]
	v_pk_add_f32 v[74:75], v[74:75], v[208:209]
	v_lshl_add_u64 v[78:79], s[2:3], 0, v[146:147]
	global_store_dwordx4 v[142:143], v[102:105], off offset:576
	global_store_dwordx4 v[110:111], v[86:89], off offset:576
	global_store_dwordx4 v[94:95], v[74:77], off offset:576
	v_pk_add_f32 v[104:105], v[120:121], v[166:167]
	v_pk_add_f32 v[102:103], v[118:119], v[164:165]
	v_pk_add_f32 v[88:89], v[108:109], v[182:183]
	v_pk_add_f32 v[86:87], v[106:107], v[180:181]
	v_pk_add_f32 v[76:77], v[92:93], v[214:215]
	v_pk_add_f32 v[74:75], v[90:91], v[212:213]
	v_lshl_add_u64 v[78:79], v[78:79], 0, v[136:137]
	v_pk_add_f32 v[128:129], v[128:129], v[144:145]
	v_pk_add_f32 v[124:125], v[124:125], v[154:155]
	v_pk_add_f32 v[122:123], v[122:123], v[152:153]
	global_store_dwordx4 v[110:111], v[102:105], off
	global_store_dwordx4 v[94:95], v[86:89], off
	global_store_dwordx4 v[78:79], v[74:77], off
	v_pk_add_f32 v[104:105], v[116:117], v[170:171]
	v_pk_add_f32 v[102:103], v[114:115], v[168:169]
	v_pk_add_f32 v[88:89], v[100:101], v[202:203]
	v_pk_add_f32 v[86:87], v[98:99], v[200:201]
	v_pk_add_f32 v[76:77], v[84:85], v[218:219]
	v_pk_add_f32 v[74:75], v[82:83], v[216:217]
	v_pk_add_f32 v[72:73], v[72:73], v[222:223]
	v_pk_add_f32 v[70:71], v[70:71], v[220:221]
	v_pk_add_f32 v[68:69], v[68:69], v[234:235]
	v_pk_add_f32 v[66:67], v[66:67], v[232:233]
	v_lshl_add_u64 v[146:147], v[140:141], 0, s[12:13]
	global_store_dwordx4 v[142:143], v[126:129], off
	global_store_dwordx4 v[142:143], v[122:125], off offset:64
	global_store_dwordx4 v[110:111], v[102:105], off offset:64
	global_store_dwordx4 v[94:95], v[86:89], off offset:64
	global_store_dwordx4 v[78:79], v[74:77], off offset:64
	global_store_dwordx4 v[78:79], v[70:73], off offset:512
	global_store_dwordx4 v[78:79], v[66:69], off offset:576
	s_mov_b64 s[12:13], 0x120000
	v_lshl_add_u64 v[144:145], v[140:141], 0, s[12:13]
	v_lshl_add_u64 v[66:67], v[138:139], 0, v[146:147]
	global_load_dwordx4 v[110:113], v[66:67], off nt
	global_load_dwordx4 v[106:109], v[66:67], off offset:64 nt
	global_load_dwordx4 v[102:105], v[66:67], off offset:512 nt
	global_load_dwordx4 v[94:97], v[66:67], off offset:576 nt
	v_lshl_add_u64 v[66:67], v[138:139], 0, v[144:145]
	s_mov_b64 s[12:13], 0x140000
	global_load_dwordx4 v[98:101], v[66:67], off nt
	global_load_dwordx4 v[90:93], v[66:67], off offset:64 nt
	global_load_dwordx4 v[82:85], v[66:67], off offset:512 nt
	global_load_dwordx4 v[74:77], v[66:67], off offset:576 nt
	v_lshl_add_u64 v[142:143], v[140:141], 0, s[12:13]
	v_lshl_add_u64 v[66:67], v[138:139], 0, v[142:143]
	s_mov_b64 s[12:13], 0x160000
	global_load_dwordx4 v[86:89], v[66:67], off nt
	global_load_dwordx4 v[78:81], v[66:67], off offset:64 nt
	global_load_dwordx4 v[70:73], v[66:67], off offset:512 nt
	s_nop 0
	global_load_dwordx4 v[66:69], v[66:67], off offset:576 nt
	v_lshl_add_u64 v[140:141], v[140:141], 0, s[12:13]
	v_lshl_add_u64 v[126:127], v[138:139], 0, v[140:141]
	global_load_dwordx4 v[122:125], v[126:127], off nt
	global_load_dwordx4 v[118:121], v[126:127], off offset:64 nt
	global_load_dwordx4 v[114:117], v[126:127], off offset:512 nt
	s_nop 0
	global_load_dwordx4 v[126:129], v[126:127], off offset:576 nt
	s_mov_b64 s[12:13], -1
	s_waitcnt vmcnt(15)
;     __device__ __forceinline__ void operator()(const f32x4 (&acc)[2][2][4][2], const Unit& u, int wr, int wc, int fr, int fq) const {
;     ...
; #pragma unroll
;             for (int m = 0; m < 4; ++m) { const size_t off = (size_t)(row0 + ai * HALF + m * 16) * D + col0;
; #pragma unroll
;                 for (int bj = 0; bj < 2; ++bj)
; #pragma unroll
;                     for (int n = 0; n < 2; ++n) *(f32x4*)(out + off + bj * HALF + n * 16) = bs[m][bj][n] + acc[ai][bj][m][n]; }
;         }
	v_pk_add_f32 v[62:63], v[62:63], v[110:111]
	v_lshl_add_u64 v[110:111], s[2:3], 0, v[146:147]
	v_lshl_add_u64 v[110:111], v[110:111], 0, v[136:137]
	s_waitcnt vmcnt(13)
	v_pk_add_f32 v[52:53], v[52:53], v[104:105]
	v_pk_add_f32 v[50:51], v[50:51], v[102:103]
	global_store_dwordx4 v[110:111], v[50:53], off offset:512
	s_waitcnt vmcnt(10)
	v_pk_add_f32 v[36:37], v[36:37], v[84:85]
	v_pk_add_f32 v[34:35], v[34:35], v[82:83]
	v_lshl_add_u64 v[50:51], s[2:3], 0, v[144:145]
	v_lshl_add_u64 v[50:51], v[50:51], 0, v[136:137]
	global_store_dwordx4 v[50:51], v[34:37], off offset:512
	s_waitcnt vmcnt(7)
	v_pk_add_f32 v[20:21], v[20:21], v[72:73]
	v_pk_add_f32 v[18:19], v[18:19], v[70:71]
	v_lshl_add_u64 v[34:35], s[2:3], 0, v[142:143]
	v_lshl_add_u64 v[34:35], v[34:35], 0, v[136:137]
	v_pk_add_f32 v[44:45], v[44:45], v[96:97]
	v_pk_add_f32 v[42:43], v[42:43], v[94:95]
	v_pk_add_f32 v[28:29], v[28:29], v[76:77]
	v_pk_add_f32 v[26:27], v[26:27], v[74:75]
	global_store_dwordx4 v[34:35], v[18:21], off offset:512
	s_waitcnt vmcnt(7)
	v_pk_add_f32 v[12:13], v[12:13], v[68:69]
	v_pk_add_f32 v[10:11], v[10:11], v[66:67]
	v_lshl_add_u64 v[18:19], s[2:3], 0, v[140:141]
	global_store_dwordx4 v[110:111], v[42:45], off offset:576
	global_store_dwordx4 v[50:51], v[26:29], off offset:576
	global_store_dwordx4 v[34:35], v[10:13], off offset:576
	v_pk_add_f32 v[44:45], v[56:57], v[100:101]
	v_pk_add_f32 v[42:43], v[54:55], v[98:99]
	v_pk_add_f32 v[28:29], v[40:41], v[88:89]
	v_pk_add_f32 v[26:27], v[38:39], v[86:87]
	s_waitcnt vmcnt(9)
	v_pk_add_f32 v[12:13], v[24:25], v[124:125]
	v_pk_add_f32 v[10:11], v[22:23], v[122:123]
	v_lshl_add_u64 v[18:19], v[18:19], 0, v[136:137]
	v_pk_add_f32 v[64:65], v[64:65], v[112:113]
	v_pk_add_f32 v[60:61], v[60:61], v[108:109]
	v_pk_add_f32 v[58:59], v[58:59], v[106:107]
	global_store_dwordx4 v[50:51], v[42:45], off
	global_store_dwordx4 v[34:35], v[26:29], off
	global_store_dwordx4 v[18:19], v[10:13], off
	v_pk_add_f32 v[44:45], v[48:49], v[92:93]
	v_pk_add_f32 v[42:43], v[46:47], v[90:91]
	v_pk_add_f32 v[28:29], v[32:33], v[80:81]
	v_pk_add_f32 v[26:27], v[30:31], v[78:79]
	s_waitcnt vmcnt(11)
	v_pk_add_f32 v[12:13], v[16:17], v[120:121]
	v_pk_add_f32 v[10:11], v[14:15], v[118:119]
	s_waitcnt vmcnt(10)
	v_pk_add_f32 v[8:9], v[8:9], v[116:117]
	v_pk_add_f32 v[6:7], v[6:7], v[114:115]
	s_waitcnt vmcnt(9)
	v_pk_add_f32 v[4:5], v[4:5], v[128:129]
	v_pk_add_f32 v[2:3], v[2:3], v[126:127]
	global_store_dwordx4 v[110:111], v[62:65], off
	global_store_dwordx4 v[110:111], v[58:61], off offset:64
	global_store_dwordx4 v[50:51], v[42:45], off offset:64
	global_store_dwordx4 v[34:35], v[26:29], off offset:64
	global_store_dwordx4 v[18:19], v[10:13], off offset:64
	global_store_dwordx4 v[18:19], v[6:9], off offset:512
	global_store_dwordx4 v[18:19], v[2:5], off offset:576
	s_cbranch_vccnz .LBB0_1276
	s_andn2_b64 vcc, exec, s[6:7]
	s_cbranch_vccnz .LBB0_1275
	s_barrier
	s_branch .LBB0_1275
